# speedup vs baseline: 1.0188x; 1.0090x over previous
.LBB0_17:
	s_lshl_b32 s14, s18, 4
	s_lshl_b32 s15, s18, 6
	s_or_b32 s21, s14, 1
	v_or_b32_e32 v48, s15, v31
	v_readlane_b32 s22, v2, s14
	v_or_b32_e32 v49, s15, v32
	v_readlane_b32 s31, v2, s21
	ds_bpermute_b32 v64, v48, v4
	v_or_b32_e32 v50, s15, v33
	v_or_b32_e32 v60, s15, v34
	v_or_b32_e32 v61, s15, v35
	ds_bpermute_b32 v65, v48, v5
	ds_bpermute_b32 v66, v49, v4
	ds_bpermute_b32 v67, v49, v5
	v_mov_b32_e32 v70, s22
	s_waitcnt vmcnt(3)
	v_fma_f32 v85, v70, v54, v58
	s_waitcnt vmcnt(0)
	v_fma_f32 v86, -v70, v3, v55
	v_mov_b32_e32 v87, s31
	v_fma_f32 v3, v70, v55, v3
	v_fma_f32 v54, -v70, v58, v54
	v_fma_f32 v91, v87, v53, v56
	v_fma_f32 v53, -v87, v56, v53
	ds_bpermute_b32 v56, v20, v54
	s_waitcnt lgkmcnt(2)
	v_mul_f32 v98, v64, v66
	s_waitcnt lgkmcnt(1)
	v_mul_f32 v64, v64, v67
	v_or_b32_e32 v51, s15, v21
	v_bitop3_b32 v59, s15, 36, v21 bitop3:0x36
	ds_bpermute_b32 v48, v48, v2
	ds_bpermute_b32 v68, v50, v4
	ds_bpermute_b32 v69, v50, v5
	ds_bpermute_b32 v77, v60, v4
	ds_bpermute_b32 v78, v60, v5
	ds_bpermute_b32 v79, v61, v4
	ds_bpermute_b32 v80, v61, v5
	v_fma_f32 v92, -v87, v57, v52
	v_fma_f32 v52, v87, v52, v57
	ds_bpermute_b32 v57, v20, v3
	s_waitcnt lgkmcnt(2)
	v_mul_f32 v99, v77, v79
	v_fma_f32 v67, -v65, v67, v98
	v_fma_f32 v64, v65, v66, v64
	v_fma_f32 v3, v48, v56, v3
	v_or_b32_e32 v62, s15, v22
	s_waitcnt lgkmcnt(1)
	v_fma_f32 v65, -v78, v80, v99
	v_mul_f32 v56, v67, v68
	ds_bpermute_b32 v49, v49, v2
	ds_bpermute_b32 v73, v51, v4 offset:32
	ds_bpermute_b32 v74, v51, v5 offset:32
	ds_bpermute_b32 v75, v59, v4
	ds_bpermute_b32 v76, v59, v5
	ds_bpermute_b32 v94, v20, v53
	ds_bpermute_b32 v95, v20, v52
	v_mul_f32 v77, v77, v80
	s_waitcnt lgkmcnt(7)
	v_fma_f32 v54, -v48, v57, v54
	v_mul_f32 v57, v67, v69
	s_waitcnt lgkmcnt(5)
	v_mul_f32 v67, v65, v73
	s_waitcnt lgkmcnt(3)
	v_mul_f32 v80, v65, v75
	s_waitcnt lgkmcnt(1)
	v_fma_f32 v52, v48, v94, v52
	v_fma_f32 v66, v78, v79, v77
	v_mul_f32 v79, v65, v74
	v_mul_f32 v65, v65, v76
	v_fma_f32 v56, -v64, v69, v56
	ds_swizzle_b32 v69, v52 offset:swizzle(BITMASK_PERM,"piipp")
	ds_bpermute_b32 v81, v62, v4 offset:56
	ds_bpermute_b32 v82, v62, v5 offset:56
	ds_bpermute_b32 v87, v20, v86
	ds_bpermute_b32 v93, v20, v85
	ds_bpermute_b32 v96, v20, v92
	ds_bpermute_b32 v97, v20, v91
	s_waitcnt lgkmcnt(3)
	v_fma_f32 v77, v48, v87, v85
	s_waitcnt lgkmcnt(2)
	v_fma_f32 v78, -v48, v93, v86
	s_waitcnt lgkmcnt(1)
	v_fma_f32 v85, v48, v96, v91
	s_waitcnt lgkmcnt(0)
	v_fma_f32 v86, -v48, v97, v92
	v_fma_f32 v48, -v48, v95, v53
	v_fma_f32 v57, v64, v68, v57
	v_fma_f32 v64, -v66, v74, v67
	v_fma_f32 v67, v66, v73, v79
	v_fma_f32 v68, -v66, v76, v80
	v_fma_f32 v65, v66, v75, v65
	ds_swizzle_b32 v66, v48 offset:swizzle(BITMASK_PERM,"piipp")
	ds_swizzle_b32 v74, v85 offset:swizzle(BITMASK_PERM,"piipp")
	v_readlane_b32 s19, v4, s14
	v_readlane_b32 s20, v5, s14
	v_bitop3_b32 v63, s15, 60, v22 bitop3:0x36
	v_readlane_b32 s29, v4, s21
	v_readlane_b32 s30, v5, s21
	v_mov_b32_e32 v71, s19
	v_mov_b32_e32 v72, s20
	ds_bpermute_b32 v83, v63, v4
	ds_bpermute_b32 v84, v63, v5
	v_mov_b32_e32 v55, s29
	v_mov_b32_e32 v58, s30
	ds_swizzle_b32 v53, v54 offset:swizzle(BITMASK_PERM,"piipp")
	ds_swizzle_b32 v73, v86 offset:swizzle(BITMASK_PERM,"piipp")
	v_mul_f32 v75, v56, v71
	v_mul_f32 v76, v56, v72
	v_mul_f32 v79, v56, v55
	v_mul_f32 v56, v56, v58
	v_mul_f32 v80, v64, v81
	v_mul_f32 v93, v64, v82
	s_waitcnt lgkmcnt(3)
	v_mul_f32 v94, v64, v83
	s_waitcnt lgkmcnt(2)
	v_mul_f32 v64, v64, v84
	v_mul_f32 v95, v68, v81
	v_mul_f32 v96, v68, v82
	v_mul_f32 v97, v68, v83
	v_mul_f32 v68, v68, v84
	ds_bpermute_b32 v50, v50, v2
	ds_swizzle_b32 v87, v3 offset:swizzle(BITMASK_PERM,"piipp")
	ds_swizzle_b32 v91, v78 offset:swizzle(BITMASK_PERM,"piipp")
	ds_swizzle_b32 v92, v77 offset:swizzle(BITMASK_PERM,"piipp")
	v_fma_f32 v72, -v57, v72, v75
	v_fma_f32 v71, v57, v71, v76
	v_fma_f32 v58, -v57, v58, v79
	v_fma_f32 v55, v57, v55, v56
	v_fma_f32 v56, -v67, v82, v80
	v_fma_f32 v57, v67, v81, v93
	v_fma_f32 v75, -v67, v84, v94
	v_fma_f32 v64, v67, v83, v64
	v_fma_f32 v67, -v65, v82, v95
	v_fma_f32 v76, v65, v81, v96
	v_fma_f32 v79, -v65, v84, v97
	v_fma_f32 v65, v65, v83, v68
	s_waitcnt lgkmcnt(1)
	v_fma_f32 v68, v49, v91, v77
	s_waitcnt lgkmcnt(0)
	v_fma_f32 v77, -v49, v92, v78
	v_fma_f32 v3, v49, v53, v3
	v_fma_f32 v53, -v49, v87, v54
	v_fma_f32 v54, v49, v73, v85
	v_fma_f32 v73, -v49, v74, v86
	v_fma_f32 v52, v49, v66, v52
	v_fma_f32 v48, -v49, v69, v48
	v_mov_b32_dpp v69, v77 quad_perm:[3,2,1,0] row_mask:0xf bank_mask:0xf bound_ctrl:1
	v_mov_b32_dpp v49, v53 quad_perm:[3,2,1,0] row_mask:0xf bank_mask:0xf bound_ctrl:1
	v_mov_b32_dpp v66, v3 quad_perm:[3,2,1,0] row_mask:0xf bank_mask:0xf bound_ctrl:1
	v_mov_b32_dpp v74, v68 quad_perm:[3,2,1,0] row_mask:0xf bank_mask:0xf bound_ctrl:1
	v_mov_b32_dpp v78, v48 quad_perm:[3,2,1,0] row_mask:0xf bank_mask:0xf bound_ctrl:1
	v_mov_b32_dpp v80, v52 quad_perm:[3,2,1,0] row_mask:0xf bank_mask:0xf bound_ctrl:1
	v_mov_b32_dpp v81, v73 quad_perm:[3,2,1,0] row_mask:0xf bank_mask:0xf bound_ctrl:1
	v_mov_b32_dpp v82, v54 quad_perm:[3,2,1,0] row_mask:0xf bank_mask:0xf bound_ctrl:1
	v_fma_f32 v68, v50, v69, v68
	v_fma_f32 v69, -v50, v74, v77
	v_fma_f32 v3, v50, v49, v3
	v_fma_f32 v49, -v50, v66, v53
	v_fma_f32 v53, v50, v81, v54
	v_fma_f32 v54, -v50, v82, v73
	v_fma_f32 v52, v50, v78, v52
	v_fma_f32 v48, -v50, v80, v48
	v_mul_f32 v66, v72, v3
	v_mul_f32 v50, v72, v49
	ds_bpermute_b32 v51, v51, v2 offset:32
	v_fma_f32 v3, -v71, v3, v50
	v_mul_f32 v50, v58, v48
	v_mul_f32 v73, v72, v69
	v_mul_f32 v72, v72, v68
	v_fma_f32 v49, v71, v49, v66
	v_mul_f32 v66, v58, v52
	v_mul_f32 v74, v58, v54
	v_mul_f32 v58, v58, v53
	s_nop 0
	v_fma_f32 v50, -v55, v52, v50
	ds_bpermute_b32 v59, v59, v2
	v_fma_f32 v48, v55, v48, v66
	v_fma_f32 v52, -v55, v53, v74
	v_fma_f32 v53, v55, v54, v58
	ds_bpermute_b32 v54, v19, v3
	ds_bpermute_b32 v55, v19, v49
	v_fma_f32 v68, -v71, v68, v73
	v_fma_f32 v69, v71, v69, v72
	ds_bpermute_b32 v58, v19, v68
	ds_bpermute_b32 v66, v19, v69
	ds_bpermute_b32 v71, v19, v50
	ds_bpermute_b32 v72, v19, v48
	ds_bpermute_b32 v73, v19, v52
	ds_bpermute_b32 v74, v19, v53
	s_waitcnt lgkmcnt(5)
	v_fma_f32 v53, v51, v58, v53
	s_waitcnt lgkmcnt(4)
	v_fma_f32 v52, -v51, v66, v52
	v_fma_f32 v48, v59, v54, v48
	v_fma_f32 v50, -v59, v55, v50
	s_waitcnt lgkmcnt(1)
	v_fma_f32 v54, v59, v73, v69
	s_waitcnt lgkmcnt(0)
	v_fma_f32 v55, -v59, v74, v68
	v_fma_f32 v49, v51, v71, v49
	v_fma_f32 v3, -v51, v72, v3
	ds_swizzle_b32 v51, v50 offset:swizzle(BITMASK_PERM,"iippp")
	ds_bpermute_b32 v60, v60, v2
	ds_swizzle_b32 v58, v48 offset:swizzle(BITMASK_PERM,"iippp")
	ds_swizzle_b32 v59, v52 offset:swizzle(BITMASK_PERM,"iippp")
	ds_swizzle_b32 v66, v53 offset:swizzle(BITMASK_PERM,"iippp")
	ds_swizzle_b32 v68, v3 offset:swizzle(BITMASK_PERM,"iippp")
	ds_swizzle_b32 v69, v49 offset:swizzle(BITMASK_PERM,"iippp")
	ds_swizzle_b32 v71, v55 offset:swizzle(BITMASK_PERM,"iippp")
	ds_swizzle_b32 v72, v54 offset:swizzle(BITMASK_PERM,"iippp")
	s_waitcnt lgkmcnt(7)
	v_fma_f32 v48, v60, v51, v48
	s_waitcnt lgkmcnt(6)
	v_fma_f32 v50, -v60, v58, v50
	s_waitcnt lgkmcnt(1)
	v_fma_f32 v51, v60, v71, v54
	s_waitcnt lgkmcnt(0)
	v_fma_f32 v54, -v60, v72, v55
	ds_swizzle_b32 v55, v50 offset:swizzle(BITMASK_PERM,"ppiip")
	ds_bpermute_b32 v61, v61, v2
	v_fma_f32 v53, v60, v59, v53
	v_fma_f32 v52, -v60, v66, v52
	v_fma_f32 v49, v60, v68, v49
	v_fma_f32 v3, -v60, v69, v3
	ds_swizzle_b32 v58, v48 offset:swizzle(BITMASK_PERM,"ppiip")
	ds_swizzle_b32 v59, v52 offset:swizzle(BITMASK_PERM,"ppiip")
	ds_swizzle_b32 v60, v53 offset:swizzle(BITMASK_PERM,"ppiip")
	ds_swizzle_b32 v66, v3 offset:swizzle(BITMASK_PERM,"ppiip")
	ds_swizzle_b32 v68, v49 offset:swizzle(BITMASK_PERM,"ppiip")
	ds_swizzle_b32 v69, v54 offset:swizzle(BITMASK_PERM,"ppiip")
	ds_bpermute_b32 v62, v62, v2 offset:56
	ds_swizzle_b32 v71, v51 offset:swizzle(BITMASK_PERM,"ppiip")
	s_waitcnt lgkmcnt(6)
	v_fma_f32 v53, v61, v59, v53
	s_waitcnt lgkmcnt(5)
	v_fma_f32 v52, -v61, v60, v52
	v_fma_f32 v48, v61, v55, v48
	v_fma_f32 v50, -v61, v58, v50
	s_waitcnt lgkmcnt(2)
	v_fma_f32 v51, v61, v69, v51
	s_waitcnt lgkmcnt(0)
	v_fma_f32 v54, -v61, v71, v54
	v_fma_f32 v49, v61, v66, v49
	v_fma_f32 v3, -v61, v68, v3
	v_mov_b32_dpp v55, v52 quad_perm:[1,0,3,2] row_mask:0xf bank_mask:0xf bound_ctrl:1
	ds_bpermute_b32 v63, v63, v2
	v_mov_b32_dpp v58, v53 quad_perm:[1,0,3,2] row_mask:0xf bank_mask:0xf bound_ctrl:1
	v_mov_b32_dpp v59, v50 quad_perm:[1,0,3,2] row_mask:0xf bank_mask:0xf bound_ctrl:1
	v_mov_b32_dpp v60, v48 quad_perm:[1,0,3,2] row_mask:0xf bank_mask:0xf bound_ctrl:1
	v_mov_b32_dpp v61, v54 quad_perm:[1,0,3,2] row_mask:0xf bank_mask:0xf bound_ctrl:1
	v_mov_b32_dpp v66, v51 quad_perm:[1,0,3,2] row_mask:0xf bank_mask:0xf bound_ctrl:1
	v_mov_b32_dpp v68, v3 quad_perm:[1,0,3,2] row_mask:0xf bank_mask:0xf bound_ctrl:1
	v_mov_b32_dpp v69, v49 quad_perm:[1,0,3,2] row_mask:0xf bank_mask:0xf bound_ctrl:1
	s_waitcnt lgkmcnt(0)
	v_fma_f32 v51, v63, v59, v51
	v_fma_f32 v54, -v63, v60, v54
	v_fma_f32 v49, v62, v55, v49
	v_fma_f32 v3, -v62, v58, v3
	v_fma_f32 v53, v63, v68, v53
	v_fma_f32 v52, -v63, v69, v52
	v_fma_f32 v48, v62, v61, v48
	v_fma_f32 v50, -v62, v66, v50
	v_mul_f32 v58, v79, v54
	v_mul_f32 v55, v56, v3
	v_mul_f32 v56, v56, v49
	v_mul_f32 v59, v79, v51
	v_mul_f32 v60, v75, v53
	s_or_b32 s23, s14, 3
	v_fma_f32 v49, -v57, v49, v55
	v_fma_f32 v3, v57, v3, v56
	v_mul_f32 v55, v67, v50
	v_mul_f32 v56, v67, v48
	v_mul_f32 v57, v75, v52
	v_fma_f32 v51, -v65, v51, v58
	v_fma_f32 v54, v65, v54, v59
	v_fma_f32 v52, v64, v52, v60
	v_fma_f32 v48, -v76, v48, v55
	v_fma_f32 v50, v76, v50, v56
	v_fma_f32 v53, -v64, v53, v57
	s_or_b32 s24, s14, 2
	v_fmac_f32_dpp v49, v49, v23 quad_perm:[1,0,3,2] row_mask:0xf bank_mask:0xf
	v_fmac_f32_dpp v48, v48, v23 quad_perm:[1,0,3,2] row_mask:0xf bank_mask:0xf
	v_fmac_f32_dpp v53, v53, v23 quad_perm:[1,0,3,2] row_mask:0xf bank_mask:0xf
	v_fmac_f32_dpp v51, v51, v23 quad_perm:[1,0,3,2] row_mask:0xf bank_mask:0xf
	v_fmac_f32_dpp v3, v3, v23 quad_perm:[1,0,3,2] row_mask:0xf bank_mask:0xf
	v_fmac_f32_dpp v50, v50, v23 quad_perm:[1,0,3,2] row_mask:0xf bank_mask:0xf
	v_fmac_f32_dpp v52, v52, v23 quad_perm:[1,0,3,2] row_mask:0xf bank_mask:0xf
	v_fmac_f32_dpp v54, v54, v23 quad_perm:[1,0,3,2] row_mask:0xf bank_mask:0xf

	v_readlane_b32 s20, v45, s23
	s_nop 1
	v_fmac_f32_dpp v49, v49, v24 quad_perm:[2,3,0,1] row_mask:0xf bank_mask:0xf
	v_fmac_f32_dpp v48, v48, v24 quad_perm:[2,3,0,1] row_mask:0xf bank_mask:0xf
	v_fmac_f32_dpp v53, v53, v24 quad_perm:[2,3,0,1] row_mask:0xf bank_mask:0xf
	v_fmac_f32_dpp v51, v51, v24 quad_perm:[2,3,0,1] row_mask:0xf bank_mask:0xf
	v_fmac_f32_dpp v3, v3, v24 quad_perm:[2,3,0,1] row_mask:0xf bank_mask:0xf
	v_fmac_f32_dpp v50, v50, v24 quad_perm:[2,3,0,1] row_mask:0xf bank_mask:0xf
	v_fmac_f32_dpp v52, v52, v24 quad_perm:[2,3,0,1] row_mask:0xf bank_mask:0xf
	v_fmac_f32_dpp v54, v54, v24 quad_perm:[2,3,0,1] row_mask:0xf bank_mask:0xf

	v_readlane_b32 s19, v45, s24
	v_readlane_b32 s15, v45, s14
	v_mov_b32_dpp v55, v49 row_half_mirror row_mask:0xf bank_mask:0xf bound_ctrl:1
	v_mov_b32_dpp v56, v48 row_half_mirror row_mask:0xf bank_mask:0xf bound_ctrl:1
	v_mov_b32_dpp v57, v53 row_half_mirror row_mask:0xf bank_mask:0xf bound_ctrl:1
	v_mov_b32_dpp v58, v51 row_half_mirror row_mask:0xf bank_mask:0xf bound_ctrl:1
	v_mov_b32_dpp v59, v3 row_half_mirror row_mask:0xf bank_mask:0xf bound_ctrl:1
	v_mov_b32_dpp v60, v50 row_half_mirror row_mask:0xf bank_mask:0xf bound_ctrl:1
	v_mov_b32_dpp v61, v52 row_half_mirror row_mask:0xf bank_mask:0xf bound_ctrl:1
	v_mov_b32_dpp v62, v54 row_half_mirror row_mask:0xf bank_mask:0xf bound_ctrl:1
	v_fmac_f32_dpp v49, v55, v25 quad_perm:[3,2,1,0] row_mask:0xf bank_mask:0xf
	v_fmac_f32_dpp v48, v56, v25 quad_perm:[3,2,1,0] row_mask:0xf bank_mask:0xf
	v_fmac_f32_dpp v53, v57, v25 quad_perm:[3,2,1,0] row_mask:0xf bank_mask:0xf
	v_fmac_f32_dpp v51, v58, v25 quad_perm:[3,2,1,0] row_mask:0xf bank_mask:0xf
	v_fmac_f32_dpp v3, v59, v25 quad_perm:[3,2,1,0] row_mask:0xf bank_mask:0xf
	v_fmac_f32_dpp v50, v60, v25 quad_perm:[3,2,1,0] row_mask:0xf bank_mask:0xf
	v_fmac_f32_dpp v52, v61, v25 quad_perm:[3,2,1,0] row_mask:0xf bank_mask:0xf
	v_fmac_f32_dpp v54, v62, v25 quad_perm:[3,2,1,0] row_mask:0xf bank_mask:0xf

	s_or_b32 s25, s14, 4
	v_fmac_f32_dpp v49, v49, v26 row_ror:8 row_mask:0xf bank_mask:0xf
	v_fmac_f32_dpp v48, v48, v26 row_ror:8 row_mask:0xf bank_mask:0xf
	v_fmac_f32_dpp v53, v53, v26 row_ror:8 row_mask:0xf bank_mask:0xf
	v_fmac_f32_dpp v51, v51, v26 row_ror:8 row_mask:0xf bank_mask:0xf
	v_fmac_f32_dpp v3, v3, v26 row_ror:8 row_mask:0xf bank_mask:0xf
	v_fmac_f32_dpp v50, v50, v26 row_ror:8 row_mask:0xf bank_mask:0xf
	v_fmac_f32_dpp v52, v52, v26 row_ror:8 row_mask:0xf bank_mask:0xf
	v_fmac_f32_dpp v54, v54, v26 row_ror:8 row_mask:0xf bank_mask:0xf

	s_or_b32 s26, s14, 5
	v_add_f32 v55, v49, v48
	v_sub_f32 v48, v49, v48
	v_add_f32 v49, v3, v50
	v_sub_f32 v3, v3, v50
	v_add_f32 v50, v53, v51
	v_sub_f32 v51, v53, v51
	v_add_f32 v53, v52, v54
	v_sub_f32 v52, v52, v54
	s_or_b32 s27, s14, 6
	v_add_f32 v54, v55, v50
	v_sub_f32 v50, v55, v50
	v_add_f32 v55, v49, v53
	v_sub_f32 v49, v49, v53
	v_add_f32 v53, v48, v51
	v_sub_f32 v48, v48, v51
	v_add_f32 v51, v3, v52
	v_sub_f32 v3, v3, v52
	s_or_b32 s28, s14, 7
	v_permlane16_swap_b32 v54, v53
	v_permlane16_swap_b32 v55, v51
	v_permlane16_swap_b32 v50, v48
	v_permlane16_swap_b32 v49, v3
	v_readlane_b32 s14, v45, s21
	s_nop 1
	v_permlane32_swap_b32 v54, v50
	v_permlane32_swap_b32 v55, v49
	v_permlane32_swap_b32 v53, v48
	v_permlane32_swap_b32 v51, v3
	v_readlane_b32 s21, v45, s25
	v_add_f32 v52, v54, v53
	v_sub_f32 v53, v54, v53
	v_add_f32 v54, v55, v51
	v_sub_f32 v51, v55, v51
	v_add_f32 v55, v50, v48
	v_sub_f32 v48, v50, v48
	v_add_f32 v50, v49, v3
	v_sub_f32 v3, v49, v3
	v_readlane_b32 s22, v45, s26
	v_add_f32 v49, v52, v55
	v_sub_f32 v52, v52, v55
	v_add_f32 v55, v54, v50
	v_sub_f32 v50, v54, v50
	v_add_f32 v54, v53, v48
	v_sub_f32 v48, v53, v48
	v_add_f32 v53, v51, v3
	v_sub_f32 v3, v51, v3
	v_mul_f32 v49, v49, v7
	v_mul_f32 v51, v55, v7
	v_mul_f32 v54, v54, v8
	v_mul_f32 v48, v48, v10
	v_mul_f32 v53, v53, v8
	v_mul_f32 v3, v3, v10
	v_mul_f32 v52, v52, v9
	v_mul_f32 v50, v50, v9
	s_nop 0
	v_fma_f32 v56, -s20, v54, v51
	v_fma_f32 v51, s20, v51, v54
	v_fma_f32 v55, s20, v53, v49
	v_fma_f32 v49, -s20, v49, v53
	v_fma_f32 v53, s20, v3, v52
	v_fma_f32 v54, -s20, v48, v50
	v_fma_f32 v48, s20, v50, v48
	v_fma_f32 v3, -s20, v52, v3
	v_mov_b32_e32 v70, s21
	v_fma_f32 v50, s19, v54, v55
	v_fma_f32 v52, -s19, v53, v56
	v_fma_f32 v53, s19, v56, v53
	v_fma_f32 v54, -s19, v55, v54
	v_fma_f32 v55, s19, v3, v51
	v_fma_f32 v56, -s19, v48, v49
	v_fma_f32 v48, s19, v49, v48
	v_fma_f32 v3, -s19, v51, v3
	v_readlane_b32 s23, v45, s27
	s_nop 1
	v_permlane32_swap_b32 v50, v53
	v_permlane32_swap_b32 v52, v54
	v_permlane32_swap_b32 v55, v48
	v_permlane32_swap_b32 v56, v3
	v_mov_b32_e32 v88, s22
	s_nop 1
	v_permlane16_swap_b32 v50, v55
	v_permlane16_swap_b32 v52, v56
	v_permlane16_swap_b32 v53, v48
	v_permlane16_swap_b32 v54, v3
	s_and_b64 vcc, exec, s[10:11]
	v_fma_f32 v51, -s14, v55, v52
	v_fma_f32 v58, s14, v52, v55
	v_fma_f32 v52, s14, v3, v53
	v_fma_f32 v55, -s14, v48, v54
	v_fma_f32 v49, s14, v56, v50
	v_fma_f32 v50, -s14, v50, v56
	v_fma_f32 v48, s14, v54, v48
	v_fma_f32 v59, -s14, v53, v3
	s_nop 0
	v_fma_f32 v3, -s15, v52, v51
	v_fma_f32 v52, s15, v51, v52
	v_fma_f32 v54, s15, v55, v49
	v_fma_f32 v56, -s15, v49, v55
	v_fma_f32 v57, -s15, v48, v50
	v_fma_f32 v53, s15, v59, v58
	v_fma_f32 v55, s15, v50, v48
	v_fma_f32 v58, -s15, v58, v59
	s_mov_b64 s[10:11], 0
	v_mul_f32_dpp v48, v54, v70 row_ror:8 row_mask:0xf bank_mask:0xf
	v_mul_f32_dpp v49, v53, v70 row_ror:8 row_mask:0xf bank_mask:0xf
	v_mul_f32_dpp v50, v52, v70 row_ror:8 row_mask:0xf bank_mask:0xf
	v_mul_f32_dpp v51, v55, v70 row_ror:8 row_mask:0xf bank_mask:0xf
	v_fmac_f32_dpp v54, v3, v70 row_ror:8 row_mask:0xf bank_mask:0xf
	v_fmac_f32_dpp v53, v57, v70 row_ror:8 row_mask:0xf bank_mask:0xf
	v_fmac_f32_dpp v52, v56, v70 row_ror:8 row_mask:0xf bank_mask:0xf
	v_fmac_f32_dpp v55, v58, v70 row_ror:8 row_mask:0xf bank_mask:0xf
	v_sub_f32 v3, v3, v48
	v_sub_f32 v57, v57, v49
	v_sub_f32 v56, v56, v50
	v_sub_f32 v58, v58, v51
	s_mov_b32 s18, 1
	v_readlane_b32 s24, v45, s28
	v_mov_b32_dpp v48, v54 row_half_mirror row_mask:0xf bank_mask:0xf bound_ctrl:1
	v_mov_b32_dpp v49, v53 row_half_mirror row_mask:0xf bank_mask:0xf bound_ctrl:1
	v_mov_b32_dpp v50, v52 row_half_mirror row_mask:0xf bank_mask:0xf bound_ctrl:1
	v_mov_b32_dpp v51, v55 row_half_mirror row_mask:0xf bank_mask:0xf bound_ctrl:1
	v_mov_b32_dpp v59, v3 row_half_mirror row_mask:0xf bank_mask:0xf bound_ctrl:1
	v_mov_b32_dpp v60, v57 row_half_mirror row_mask:0xf bank_mask:0xf bound_ctrl:1
	v_mov_b32_dpp v61, v56 row_half_mirror row_mask:0xf bank_mask:0xf bound_ctrl:1
	v_mov_b32_dpp v62, v58 row_half_mirror row_mask:0xf bank_mask:0xf bound_ctrl:1
	v_mul_f32_dpp v63, v48, v88 quad_perm:[3,2,1,0] row_mask:0xf bank_mask:0xf
	v_mul_f32_dpp v64, v49, v88 quad_perm:[3,2,1,0] row_mask:0xf bank_mask:0xf
	v_mul_f32_dpp v65, v50, v88 quad_perm:[3,2,1,0] row_mask:0xf bank_mask:0xf
	v_mul_f32_dpp v66, v51, v88 quad_perm:[3,2,1,0] row_mask:0xf bank_mask:0xf
	v_fmac_f32_dpp v54, v59, v88 quad_perm:[3,2,1,0] row_mask:0xf bank_mask:0xf
	v_fmac_f32_dpp v53, v60, v88 quad_perm:[3,2,1,0] row_mask:0xf bank_mask:0xf
	v_fmac_f32_dpp v52, v61, v88 quad_perm:[3,2,1,0] row_mask:0xf bank_mask:0xf
	v_fmac_f32_dpp v55, v62, v88 quad_perm:[3,2,1,0] row_mask:0xf bank_mask:0xf
	v_sub_f32 v3, v3, v63
	v_sub_f32 v57, v57, v64
	v_sub_f32 v56, v56, v65
	v_sub_f32 v58, v58, v66
	v_mov_b32_e32 v89, s23
	v_mul_f32_dpp v48, v54, v89 quad_perm:[2,3,0,1] row_mask:0xf bank_mask:0xf
	v_mul_f32_dpp v49, v53, v89 quad_perm:[2,3,0,1] row_mask:0xf bank_mask:0xf
	v_mul_f32_dpp v50, v52, v89 quad_perm:[2,3,0,1] row_mask:0xf bank_mask:0xf
	v_mul_f32_dpp v51, v55, v89 quad_perm:[2,3,0,1] row_mask:0xf bank_mask:0xf
	v_fmac_f32_dpp v54, v3, v89 quad_perm:[2,3,0,1] row_mask:0xf bank_mask:0xf
	v_fmac_f32_dpp v53, v57, v89 quad_perm:[2,3,0,1] row_mask:0xf bank_mask:0xf
	v_fmac_f32_dpp v52, v56, v89 quad_perm:[2,3,0,1] row_mask:0xf bank_mask:0xf
	v_fmac_f32_dpp v55, v58, v89 quad_perm:[2,3,0,1] row_mask:0xf bank_mask:0xf
	v_sub_f32 v3, v3, v48
	v_sub_f32 v57, v57, v49
	v_sub_f32 v56, v56, v50
	v_sub_f32 v58, v58, v51
	v_mov_b32_e32 v90, s24
	v_mul_f32_dpp v48, v54, v90 quad_perm:[1,0,3,2] row_mask:0xf bank_mask:0xf
	v_mul_f32_dpp v49, v53, v90 quad_perm:[1,0,3,2] row_mask:0xf bank_mask:0xf
	v_mul_f32_dpp v50, v52, v90 quad_perm:[1,0,3,2] row_mask:0xf bank_mask:0xf
	v_mul_f32_dpp v51, v55, v90 quad_perm:[1,0,3,2] row_mask:0xf bank_mask:0xf
	v_fmac_f32_dpp v54, v3, v90 quad_perm:[1,0,3,2] row_mask:0xf bank_mask:0xf
	v_fmac_f32_dpp v53, v57, v90 quad_perm:[1,0,3,2] row_mask:0xf bank_mask:0xf
	v_fmac_f32_dpp v52, v56, v90 quad_perm:[1,0,3,2] row_mask:0xf bank_mask:0xf
	v_fmac_f32_dpp v55, v58, v90 quad_perm:[1,0,3,2] row_mask:0xf bank_mask:0xf
	v_sub_f32 v3, v3, v48
	v_sub_f32 v57, v57, v49
	v_sub_f32 v56, v56, v50
	v_sub_f32 v58, v58, v51
	s_cbranch_vccnz .LBB0_17
	s_mov_b64 s[10:11], -1
	s_and_b64 vcc, exec, s[8:9]
	v_mul_f32_e32 v2, v46, v47
	v_mul_f32 v51, v54, v2
	v_mul_f32 v50, v3, v2
	v_mul_f32 v49, v53, v2
	v_mul_f32 v48, v57, v2
	v_mul_f32 v47, v52, v2
	v_mul_f32 v46, v56, v2
	v_mul_f32 v45, v55, v2
	v_mul_f32 v5, v58, v2
	s_cbranch_vccz .LBB0_11
	v_mov_b32_e32 v53, 1.0
	v_mov_b32_e32 v55, 0
	v_mov_b32_e32 v4, 0
	v_mov_b32_e32 v52, 0
	v_mov_b32_e32 v2, 0
	v_mov_b32_e32 v3, 0
	s_and_saveexec_b64 s[8:9], s[0:1]
	s_cbranch_execz .LBB0_23
	ds_read_b32 v4, v28 offset:264
	ds_read2_b32 v[2:3], v28 offset0:64 offset1:65
	v_mov_b32_e32 v52, 0
	v_mov_b32_e32 v53, 1.0
	s_waitcnt lgkmcnt(1)
	v_cndmask_b32_e64 v4, v4, -v4, s[2:3]
	s_waitcnt lgkmcnt(0)
	v_add_f32_e32 v3, v3, v4
	v_mul_f32_e32 v3, 0.15915494, v3
	v_cos_f32_e32 v4, v3
	v_sin_f32_e32 v54, v3
	v_cmp_gt_f32_e32 vcc, 0, v4
	s_nop 1
	v_cndmask_b32_e32 v3, v43, v44, vcc
	v_cmp_lt_f32_e64 vcc, |v4|, s16
	s_nop 1
	v_cndmask_b32_e32 v4, v4, v3, vcc
	v_div_scale_f32 v3, s[10:11], v4, v4, v54
	v_rcp_f32_e32 v56, v3
	v_div_scale_f32 v57, vcc, v54, v4, v54
	v_fma_f32 v58, -v3, v56, 1.0
	v_fmac_f32_e32 v56, v58, v56
	v_mul_f32_e32 v58, v57, v56
	v_fma_f32 v59, -v3, v58, v57
	v_fmac_f32_e32 v58, v59, v56
	v_fma_f32 v3, -v3, v58, v57
	v_div_fmas_f32 v56, v3, v56, v58
	s_and_saveexec_b64 s[10:11], s[6:7]
	s_cbranch_execz .LBB0_22
	ds_read_b32 v3, v29 offset:352
	s_waitcnt lgkmcnt(0)
	v_mul_f32_e32 v3, 0.5, v3
	v_mul_f32_e32 v3, 0.15915494, v3
	v_cos_f32_e32 v52, v3
	v_sin_f32_e32 v3, v3
	v_cmp_gt_f32_e32 vcc, 0, v52
	s_nop 1
	v_cndmask_b32_e32 v53, v43, v44, vcc
	v_cmp_lt_f32_e64 vcc, |v52|, s16
	s_nop 1
	v_cndmask_b32_e32 v53, v52, v53, vcc
	v_div_scale_f32 v52, s[14:15], v53, v53, v3
	v_rcp_f32_e32 v57, v52
	v_div_scale_f32 v58, vcc, v3, v53, v3
	v_fma_f32 v59, -v52, v57, 1.0
	v_fmac_f32_e32 v57, v59, v57
	v_mul_f32_e32 v59, v58, v57
	v_fma_f32 v60, -v52, v59, v58
	v_fmac_f32_e32 v59, v60, v57
	v_fma_f32 v52, -v52, v59, v58
	v_div_fmas_f32 v52, v52, v57, v59
	v_div_fixup_f32 v52, v52, v53, v3

.LBB0_24:
	s_lshl_b32 s10, s14, 4
	s_lshl_b32 s11, s14, 6
	v_cndmask_b32_e64 v71, 0, 1, s[8:9]
	s_or_b32 s20, s10, 1
	v_or_b32_e32 v73, s11, v36
	v_cmp_ne_u32_e32 vcc, 1, v71
	v_readlane_b32 s28, v4, s10
	v_or_b32_e32 v71, s11, v21
	v_or_b32_e32 v74, s11, v37
	v_readlane_b32 s31, v4, s20
	ds_bpermute_b32 v84, v73, v2
	v_bitop3_b32 v72, s11, 12, v21 bitop3:0x36
	v_or_b32_e32 v75, s11, v38
	v_or_b32_e32 v76, s11, v39
	ds_bpermute_b32 v78, v71, v2 offset:8
	ds_bpermute_b32 v79, v71, v3 offset:8
	ds_bpermute_b32 v80, v71, v4 offset:8
	ds_bpermute_b32 v85, v73, v3
	ds_bpermute_b32 v87, v74, v2
	ds_bpermute_b32 v88, v74, v3
	v_mov_b32_e32 v71, s28
	v_fma_f32 v98, v71, v67, v70
	v_fma_f32 v99, -v71, v68, v69
	v_fma_f32 v100, v71, v65, v64
	v_fma_f32 v101, -v71, v66, v55
	v_mov_b32_e32 v102, s31
	v_fma_f32 v68, v71, v69, v68
	v_fma_f32 v67, -v71, v70, v67
	v_fma_f32 v55, v71, v55, v66
	v_fma_f32 v64, -v71, v64, v65
	v_fma_f32 v107, v102, v60, v63
	v_fma_f32 v109, v102, v56, v59
	v_fma_f32 v110, -v102, v57, v58
	v_fma_f32 v60, -v102, v63, v60
	v_fma_f32 v57, v102, v58, v57
	v_fma_f32 v56, -v102, v59, v56
	ds_bpermute_b32 v58, v19, v67
	ds_bpermute_b32 v59, v19, v68
	ds_bpermute_b32 v63, v19, v55
	s_waitcnt lgkmcnt(4)
	v_mul_f32 v122, v84, v87
	s_waitcnt lgkmcnt(3)
	v_mul_f32 v84, v84, v88
	s_or_b32 s21, s10, 8
	s_or_b32 s15, s10, 9
	v_readlane_b32 s27, v3, s10
	v_or_b32_e32 v77, s11, v40
	ds_bpermute_b32 v81, v72, v2
	ds_bpermute_b32 v83, v72, v4
	ds_bpermute_b32 v92, v75, v2
	ds_bpermute_b32 v93, v75, v3
	ds_bpermute_b32 v94, v76, v2
	ds_bpermute_b32 v95, v76, v3
	v_fma_f32 v108, -v102, v61, v62
	v_fma_f32 v61, v102, v62, v61
	ds_bpermute_b32 v62, v19, v64
	s_waitcnt lgkmcnt(2)
	v_mul_f32 v123, v92, v94
	v_fma_f32 v88, -v85, v88, v122
	v_fma_f32 v84, v85, v87, v84
	v_fma_f32 v63, -v83, v63, v67
	v_fma_f32 v55, v80, v58, v55
	v_fma_f32 v58, -v80, v59, v64
	s_waitcnt lgkmcnt(1)
	v_fma_f32 v85, -v93, v95, v123
	v_mul_f32 v59, v88, v78
	v_mul_f32 v64, v88, v79
	v_mul_f32 v67, v88, v81
	v_readlane_b32 s19, v2, s10
	v_readlane_b32 s29, v2, s20
	v_readlane_b32 s30, v3, s20
	ds_bpermute_b32 v82, v72, v3
	v_mov_b32_e32 v91, s27
	v_readlane_b32 s27, v2, s21
	v_readlane_b32 s28, v2, s15
	v_readlane_b32 s33, v3, s21
	v_readlane_b32 s34, v3, s15
	ds_bpermute_b32 v96, v77, v2
	ds_bpermute_b32 v97, v77, v3
	ds_bpermute_b32 v112, v19, v101
	ds_bpermute_b32 v113, v19, v100
	ds_bpermute_b32 v114, v19, v60
	ds_bpermute_b32 v115, v19, v61
	ds_bpermute_b32 v116, v19, v56
	ds_bpermute_b32 v117, v19, v57
	ds_bpermute_b32 v118, v19, v108
	ds_bpermute_b32 v119, v19, v107
	ds_bpermute_b32 v120, v19, v110
	v_mul_f32 v92, v92, v95
	s_waitcnt lgkmcnt(12)
	v_fma_f32 v62, v83, v62, v68
	s_waitcnt lgkmcnt(11)
	v_mul_f32 v68, v88, v82
	s_waitcnt lgkmcnt(10)
	v_mul_f32 v88, v85, v96
	s_waitcnt lgkmcnt(9)
	v_mul_f32 v85, v85, v97
	v_fma_f32 v59, -v84, v79, v59
	v_fma_f32 v87, v93, v94, v92
	v_fma_f32 v64, v84, v78, v64
	v_fma_f32 v67, -v84, v82, v67
	ds_bpermute_b32 v86, v73, v4
	v_fma_f32 v78, -v87, v97, v88
	v_mov_b32_e32 v90, s19
	v_mov_b32_e32 v65, s29
	v_mov_b32_e32 v66, s30
	v_mov_b32_e32 v103, s27
	v_mov_b32_e32 v104, s33
	v_mov_b32_e32 v105, s28
	v_mov_b32_e32 v106, s34
	ds_bpermute_b32 v102, v19, v99
	ds_bpermute_b32 v111, v19, v98
	ds_bpermute_b32 v121, v19, v109
	s_waitcnt lgkmcnt(12)
	v_fma_f32 v92, v83, v112, v98
	s_waitcnt lgkmcnt(11)
	v_fma_f32 v93, -v83, v113, v99
	s_waitcnt lgkmcnt(2)
	v_fma_f32 v94, v80, v102, v100
	s_waitcnt lgkmcnt(1)
	v_fma_f32 v95, -v80, v111, v101
	v_fma_f32 v98, v83, v120, v107
	s_waitcnt lgkmcnt(0)
	v_fma_f32 v99, -v83, v121, v108
	v_fma_f32 v100, v80, v118, v109
	v_fma_f32 v101, -v80, v119, v110
	v_fma_f32 v61, v83, v116, v61
	v_fma_f32 v60, -v83, v117, v60
	v_fma_f32 v57, v80, v114, v57
	v_fma_f32 v56, -v80, v115, v56
	ds_swizzle_b32 v80, v58 offset:swizzle(BITMASK_PERM,"iippp")
	ds_swizzle_b32 v83, v55 offset:swizzle(BITMASK_PERM,"iippp")
	v_fma_f32 v68, v84, v81, v68
	v_fma_f32 v79, v87, v96, v85
	ds_swizzle_b32 v81, v56 offset:swizzle(BITMASK_PERM,"iippp")
	ds_swizzle_b32 v82, v57 offset:swizzle(BITMASK_PERM,"iippp")
	ds_swizzle_b32 v84, v60 offset:swizzle(BITMASK_PERM,"iippp")
	ds_swizzle_b32 v85, v61 offset:swizzle(BITMASK_PERM,"iippp")
	ds_swizzle_b32 v87, v101 offset:swizzle(BITMASK_PERM,"iippp")
	ds_swizzle_b32 v88, v100 offset:swizzle(BITMASK_PERM,"iippp")
	v_mul_f32 v112, v59, v90
	v_mul_f32 v113, v59, v91
	v_mul_f32 v114, v59, v65
	v_mul_f32 v59, v59, v66
	v_mul_f32 v115, v67, v90
	v_mul_f32 v116, v67, v91
	v_mul_f32 v117, v67, v65
	v_mul_f32 v67, v67, v66
	v_mul_f32 v118, v78, v103
	v_mul_f32 v119, v78, v104
	v_mul_f32 v120, v78, v105
	v_mul_f32 v78, v78, v106
	ds_swizzle_b32 v102, v63 offset:swizzle(BITMASK_PERM,"iippp")
	ds_swizzle_b32 v107, v62 offset:swizzle(BITMASK_PERM,"iippp")
	ds_swizzle_b32 v108, v95 offset:swizzle(BITMASK_PERM,"iippp")
	ds_swizzle_b32 v109, v94 offset:swizzle(BITMASK_PERM,"iippp")
	ds_swizzle_b32 v110, v93 offset:swizzle(BITMASK_PERM,"iippp")
	ds_swizzle_b32 v111, v92 offset:swizzle(BITMASK_PERM,"iippp")
	ds_swizzle_b32 v96, v99 offset:swizzle(BITMASK_PERM,"iippp")
	ds_swizzle_b32 v97, v98 offset:swizzle(BITMASK_PERM,"iippp")
	v_fma_f32 v112, -v64, v91, v112
	v_fma_f32 v113, v64, v90, v113
	v_fma_f32 v114, -v64, v66, v114
	v_fma_f32 v59, v64, v65, v59
	v_fma_f32 v64, -v68, v91, v115
	v_fma_f32 v90, v68, v90, v116
	v_fma_f32 v66, -v68, v66, v117
	v_fma_f32 v65, v68, v65, v67
	v_fma_f32 v67, -v79, v104, v118
	v_fma_f32 v68, v79, v103, v119
	v_fma_f32 v91, -v79, v106, v120
	v_fma_f32 v78, v79, v105, v78
	s_waitcnt lgkmcnt(3)
	v_fma_f32 v79, v86, v110, v92
	s_waitcnt lgkmcnt(2)
	v_fma_f32 v92, -v86, v111, v93
	v_fma_f32 v93, v86, v108, v94
	v_fma_f32 v94, -v86, v109, v95
	v_fma_f32 v62, v86, v102, v62
	v_fma_f32 v63, -v86, v107, v63
	v_fma_f32 v55, v86, v80, v55
	v_fma_f32 v58, -v86, v83, v58
	s_waitcnt lgkmcnt(1)
	v_fma_f32 v80, v86, v96, v98
	s_waitcnt lgkmcnt(0)
	v_fma_f32 v83, -v86, v97, v99
	v_fma_f32 v87, v86, v87, v100
	v_fma_f32 v88, -v86, v88, v101
	v_fma_f32 v61, v86, v84, v61
	v_fma_f32 v60, -v86, v85, v60
	v_fma_f32 v57, v86, v81, v57
	v_fma_f32 v56, -v86, v82, v56
	ds_swizzle_b32 v81, v58 offset:swizzle(BITMASK_PERM,"ppiip")
	ds_swizzle_b32 v82, v55 offset:swizzle(BITMASK_PERM,"ppiip")
	ds_swizzle_b32 v84, v63 offset:swizzle(BITMASK_PERM,"ppiip")
	ds_swizzle_b32 v85, v62 offset:swizzle(BITMASK_PERM,"ppiip")
	ds_swizzle_b32 v86, v94 offset:swizzle(BITMASK_PERM,"ppiip")
	ds_swizzle_b32 v95, v93 offset:swizzle(BITMASK_PERM,"ppiip")
	ds_bpermute_b32 v89, v74, v4
	v_readlane_b32 s35, v4, s21
	v_readlane_b32 s36, v4, s15
	ds_swizzle_b32 v96, v92 offset:swizzle(BITMASK_PERM,"ppiip")
	ds_swizzle_b32 v97, v79 offset:swizzle(BITMASK_PERM,"ppiip")
	ds_swizzle_b32 v98, v56 offset:swizzle(BITMASK_PERM,"ppiip")
	ds_swizzle_b32 v99, v57 offset:swizzle(BITMASK_PERM,"ppiip")
	ds_swizzle_b32 v100, v60 offset:swizzle(BITMASK_PERM,"ppiip")
	ds_swizzle_b32 v101, v61 offset:swizzle(BITMASK_PERM,"ppiip")
	ds_swizzle_b32 v102, v88 offset:swizzle(BITMASK_PERM,"ppiip")
	ds_swizzle_b32 v103, v87 offset:swizzle(BITMASK_PERM,"ppiip")
	ds_swizzle_b32 v104, v83 offset:swizzle(BITMASK_PERM,"ppiip")
	ds_swizzle_b32 v105, v80 offset:swizzle(BITMASK_PERM,"ppiip")
	s_waitcnt lgkmcnt(9)
	v_fma_f32 v79, v89, v96, v79
	s_waitcnt lgkmcnt(8)
	v_fma_f32 v92, -v89, v97, v92
	v_fma_f32 v86, v89, v86, v93
	v_fma_f32 v93, -v89, v95, v94
	v_fma_f32 v62, v89, v84, v62
	v_fma_f32 v63, -v89, v85, v63
	v_fma_f32 v55, v89, v81, v55
	v_fma_f32 v58, -v89, v82, v58
	s_waitcnt lgkmcnt(1)
	v_fma_f32 v80, v89, v104, v80
	s_waitcnt lgkmcnt(0)
	v_fma_f32 v81, -v89, v105, v83
	v_fma_f32 v82, v89, v102, v87
	v_fma_f32 v83, -v89, v103, v88
	v_fma_f32 v61, v89, v100, v61
	v_fma_f32 v60, -v89, v101, v60
	v_fma_f32 v57, v89, v98, v57
	v_fma_f32 v56, -v89, v99, v56
	v_mul_f32 v84, v112, v58
	v_mul_f32 v85, v112, v55
	v_mul_f32 v87, v64, v63
	v_mul_f32 v88, v64, v62
	v_mul_f32 v95, v64, v92
	v_mul_f32 v64, v64, v79
	v_mov_b32_e32 v69, s35
	v_mov_b32_e32 v70, s36
	v_mul_f32 v89, v112, v93
	v_mul_f32 v94, v112, v86
	v_fma_f32 v55, -v113, v55, v84
	v_fma_f32 v58, v113, v58, v85
	v_fma_f32 v62, -v90, v62, v87
	v_fma_f32 v63, v90, v63, v88
	v_mul_f32 v84, v114, v56
	v_mul_f32 v85, v114, v57
	v_mul_f32 v87, v66, v60
	v_mul_f32 v88, v66, v61
	v_mul_f32 v96, v114, v83
	v_mul_f32 v97, v114, v82
	v_mul_f32 v98, v66, v81
	v_mul_f32 v66, v66, v80
	v_fma_f32 v86, -v113, v86, v89
	v_fma_f32 v79, -v90, v79, v95
	v_fma_f32 v64, v90, v92, v64
	v_fma_f32 v57, -v59, v57, v84
	v_fma_f32 v56, v59, v56, v85
	v_fma_f32 v61, -v65, v61, v87
	v_fma_f32 v60, v65, v60, v88
	v_fma_f32 v82, -v59, v82, v96
	v_fma_f32 v59, v59, v83, v97
	v_fma_f32 v80, -v65, v80, v98
	v_fma_f32 v65, v65, v81, v66
	ds_bpermute_b32 v75, v75, v4
	v_fma_f32 v89, v113, v93, v94
	v_fma_f32 v66, v69, v82, v64
	v_fma_f32 v81, -v69, v59, v79
	v_fma_f32 v84, -v70, v65, v86
	v_fma_f32 v65, v70, v86, v65
	v_fma_f32 v59, v69, v79, v59
	v_fma_f32 v83, v70, v80, v89
	v_fma_f32 v80, -v70, v89, v80
	v_fma_f32 v64, -v69, v64, v82
	v_fma_f32 v79, v69, v55, v60
	v_fma_f32 v82, -v69, v58, v61
	v_fma_f32 v85, v70, v62, v56
	v_fma_f32 v86, -v70, v63, v57
	v_fma_f32 v57, v70, v57, v63
	v_fma_f32 v56, -v70, v56, v62
	v_fma_f32 v58, v69, v61, v58
	v_fma_f32 v55, -v69, v60, v55
	ds_bpermute_b32 v60, v20, v55
	ds_bpermute_b32 v61, v20, v58
	ds_bpermute_b32 v62, v20, v56
	ds_bpermute_b32 v63, v20, v57
	ds_bpermute_b32 v69, v20, v86
	ds_bpermute_b32 v70, v20, v85
	ds_bpermute_b32 v87, v20, v82
	ds_bpermute_b32 v92, v20, v80
	ds_bpermute_b32 v88, v20, v79
	ds_bpermute_b32 v89, v20, v64
	ds_bpermute_b32 v90, v20, v59
	ds_bpermute_b32 v93, v20, v81
	ds_bpermute_b32 v94, v20, v66
	ds_bpermute_b32 v95, v20, v84
	ds_bpermute_b32 v96, v20, v83
	ds_bpermute_b32 v97, v20, v65
	s_waitcnt lgkmcnt(4)
	v_fma_f32 v66, v75, v93, v66
	s_waitcnt lgkmcnt(3)
	v_fma_f32 v81, -v75, v94, v81
	s_waitcnt lgkmcnt(2)
	v_fma_f32 v83, v75, v95, v83
	s_waitcnt lgkmcnt(1)
	v_fma_f32 v84, -v75, v96, v84
	v_fma_f32 v65, v75, v92, v65
	s_waitcnt lgkmcnt(0)
	v_fma_f32 v80, -v75, v97, v80
	v_fma_f32 v59, v75, v89, v59
	v_fma_f32 v64, -v75, v90, v64
	v_fma_f32 v79, v75, v87, v79
	v_fma_f32 v82, -v75, v88, v82
	v_fma_f32 v69, v75, v69, v85
	v_fma_f32 v70, -v75, v70, v86
	v_fma_f32 v57, v75, v62, v57
	v_fma_f32 v56, -v75, v63, v56
	v_fma_f32 v58, v75, v60, v58
	v_fma_f32 v55, -v75, v61, v55
	ds_swizzle_b32 v60, v55 offset:swizzle(BITMASK_PERM,"piipp")
	ds_swizzle_b32 v61, v58 offset:swizzle(BITMASK_PERM,"piipp")
	ds_swizzle_b32 v62, v56 offset:swizzle(BITMASK_PERM,"piipp")
	ds_swizzle_b32 v63, v57 offset:swizzle(BITMASK_PERM,"piipp")
	ds_swizzle_b32 v75, v70 offset:swizzle(BITMASK_PERM,"piipp")
	ds_swizzle_b32 v85, v69 offset:swizzle(BITMASK_PERM,"piipp")
	ds_swizzle_b32 v86, v82 offset:swizzle(BITMASK_PERM,"piipp")
	ds_swizzle_b32 v87, v79 offset:swizzle(BITMASK_PERM,"piipp")
	ds_swizzle_b32 v92, v81 offset:swizzle(BITMASK_PERM,"piipp")
	ds_bpermute_b32 v76, v76, v4
	ds_swizzle_b32 v88, v64 offset:swizzle(BITMASK_PERM,"piipp")
	ds_swizzle_b32 v89, v59 offset:swizzle(BITMASK_PERM,"piipp")
	ds_swizzle_b32 v90, v80 offset:swizzle(BITMASK_PERM,"piipp")
	ds_swizzle_b32 v93, v66 offset:swizzle(BITMASK_PERM,"piipp")
	ds_swizzle_b32 v94, v84 offset:swizzle(BITMASK_PERM,"piipp")
	ds_swizzle_b32 v95, v83 offset:swizzle(BITMASK_PERM,"piipp")
	ds_bpermute_b32 v77, v77, v4
	ds_swizzle_b32 v96, v65 offset:swizzle(BITMASK_PERM,"piipp")
	s_waitcnt lgkmcnt(8)
	v_fma_f32 v66, v76, v92, v66
	s_waitcnt lgkmcnt(4)
	v_fma_f32 v81, -v76, v93, v81
	s_waitcnt lgkmcnt(3)
	v_fma_f32 v83, v76, v94, v83
	s_waitcnt lgkmcnt(2)
	v_fma_f32 v84, -v76, v95, v84
	v_fma_f32 v65, v76, v90, v65
	s_waitcnt lgkmcnt(0)
	v_fma_f32 v80, -v76, v96, v80
	v_fma_f32 v59, v76, v88, v59
	v_fma_f32 v64, -v76, v89, v64
	v_fma_f32 v79, v76, v86, v79
	v_fma_f32 v82, -v76, v87, v82
	v_fma_f32 v69, v76, v75, v69
	v_fma_f32 v70, -v76, v85, v70
	v_fma_f32 v57, v76, v62, v57
	v_fma_f32 v56, -v76, v63, v56
	v_fma_f32 v58, v76, v60, v58
	v_fma_f32 v55, -v76, v61, v55
	s_nop 1
	v_mov_b32_dpp v85, v82 quad_perm:[3,2,1,0] row_mask:0xf bank_mask:0xf bound_ctrl:1
	v_mov_b32_dpp v75, v70 quad_perm:[3,2,1,0] row_mask:0xf bank_mask:0xf bound_ctrl:1
	v_mov_b32_dpp v60, v55 quad_perm:[3,2,1,0] row_mask:0xf bank_mask:0xf bound_ctrl:1
	v_mov_b32_dpp v61, v58 quad_perm:[3,2,1,0] row_mask:0xf bank_mask:0xf bound_ctrl:1
	v_mov_b32_dpp v62, v56 quad_perm:[3,2,1,0] row_mask:0xf bank_mask:0xf bound_ctrl:1
	v_mov_b32_dpp v63, v57 quad_perm:[3,2,1,0] row_mask:0xf bank_mask:0xf bound_ctrl:1
	v_mov_b32_dpp v86, v79 quad_perm:[3,2,1,0] row_mask:0xf bank_mask:0xf bound_ctrl:1
	v_mov_b32_dpp v87, v64 quad_perm:[3,2,1,0] row_mask:0xf bank_mask:0xf bound_ctrl:1
	v_mov_b32_dpp v92, v84 quad_perm:[3,2,1,0] row_mask:0xf bank_mask:0xf bound_ctrl:1
	v_mov_b32_dpp v76, v69 quad_perm:[3,2,1,0] row_mask:0xf bank_mask:0xf bound_ctrl:1
	v_mov_b32_dpp v88, v59 quad_perm:[3,2,1,0] row_mask:0xf bank_mask:0xf bound_ctrl:1
	v_mov_b32_dpp v89, v80 quad_perm:[3,2,1,0] row_mask:0xf bank_mask:0xf bound_ctrl:1
	v_mov_b32_dpp v90, v65 quad_perm:[3,2,1,0] row_mask:0xf bank_mask:0xf bound_ctrl:1
	v_mov_b32_dpp v93, v83 quad_perm:[3,2,1,0] row_mask:0xf bank_mask:0xf bound_ctrl:1
	v_mov_b32_dpp v94, v81 quad_perm:[3,2,1,0] row_mask:0xf bank_mask:0xf bound_ctrl:1
	v_mov_b32_dpp v95, v66 quad_perm:[3,2,1,0] row_mask:0xf bank_mask:0xf bound_ctrl:1
	v_fma_f32 v66, v77, v94, v66
	v_fma_f32 v81, -v77, v95, v81
	v_fma_f32 v83, v77, v92, v83
	v_fma_f32 v84, -v77, v93, v84
	v_fma_f32 v65, v77, v89, v65
	v_fma_f32 v80, -v77, v90, v80
	v_fma_f32 v59, v77, v87, v59
	v_fma_f32 v64, -v77, v88, v64
	v_fma_f32 v79, v77, v85, v79
	v_fma_f32 v82, -v77, v86, v82
	v_fma_f32 v69, v77, v75, v69
	v_fma_f32 v70, -v77, v76, v70
	v_fma_f32 v57, v77, v62, v57
	v_fma_f32 v56, -v77, v63, v56
	v_fma_f32 v58, v77, v60, v58
	v_fma_f32 v55, -v77, v61, v55
	v_mul_f32 v77, v67, v82
	v_mul_f32 v75, v91, v70
	v_mul_f32 v63, v91, v57
	v_mul_f32 v62, v91, v56
	v_mul_f32 v61, v67, v58
	v_mul_f32 v60, v67, v55
	v_mul_f32 v85, v67, v79
	v_mul_f32 v86, v67, v64
	v_mul_f32 v87, v67, v59
	v_mul_f32 v92, v67, v81
	v_mul_f32 v67, v67, v66
	v_mul_f32 v76, v91, v69
	v_mul_f32 v88, v91, v80
	v_mul_f32 v89, v91, v65
	v_mul_f32 v90, v91, v84
	v_mul_f32 v91, v91, v83
	v_fma_f32 v58, -v68, v58, v60
	v_fma_f32 v55, v68, v55, v61
	v_fma_f32 v57, -v78, v57, v62
	v_fma_f32 v56, v78, v56, v63
	v_fma_f32 v60, -v78, v69, v75
	v_fma_f32 v61, v78, v70, v76
	v_fma_f32 v62, -v68, v79, v77
	v_fma_f32 v63, v68, v82, v85
	v_fma_f32 v59, -v68, v59, v86
	v_fma_f32 v64, v68, v64, v87
	v_fma_f32 v65, -v78, v65, v88
	v_fma_f32 v69, v78, v80, v89
	v_fma_f32 v70, -v78, v83, v90
	v_fma_f32 v75, v78, v84, v91
	v_fma_f32 v66, -v68, v66, v92
	v_fma_f32 v67, v68, v81, v67
	s_nop 0
	s_nop 1
	v_fmac_f32_dpp v58, v58, v23 quad_perm:[1,0,3,2] row_mask:0xf bank_mask:0xf
	v_fmac_f32_dpp v57, v57, v23 quad_perm:[1,0,3,2] row_mask:0xf bank_mask:0xf
	v_fmac_f32_dpp v60, v60, v23 quad_perm:[1,0,3,2] row_mask:0xf bank_mask:0xf
	v_fmac_f32_dpp v62, v62, v23 quad_perm:[1,0,3,2] row_mask:0xf bank_mask:0xf
	v_fmac_f32_dpp v55, v55, v23 quad_perm:[1,0,3,2] row_mask:0xf bank_mask:0xf
	v_fmac_f32_dpp v56, v56, v23 quad_perm:[1,0,3,2] row_mask:0xf bank_mask:0xf
	v_fmac_f32_dpp v61, v61, v23 quad_perm:[1,0,3,2] row_mask:0xf bank_mask:0xf
	v_fmac_f32_dpp v63, v63, v23 quad_perm:[1,0,3,2] row_mask:0xf bank_mask:0xf

	s_or_b32 s18, s10, 4
	v_fmac_f32_dpp v59, v59, v23 quad_perm:[1,0,3,2] row_mask:0xf bank_mask:0xf
	v_fmac_f32_dpp v65, v65, v23 quad_perm:[1,0,3,2] row_mask:0xf bank_mask:0xf
	v_fmac_f32_dpp v70, v70, v23 quad_perm:[1,0,3,2] row_mask:0xf bank_mask:0xf
	v_fmac_f32_dpp v66, v66, v23 quad_perm:[1,0,3,2] row_mask:0xf bank_mask:0xf
	v_fmac_f32_dpp v64, v64, v23 quad_perm:[1,0,3,2] row_mask:0xf bank_mask:0xf
	v_fmac_f32_dpp v69, v69, v23 quad_perm:[1,0,3,2] row_mask:0xf bank_mask:0xf
	v_fmac_f32_dpp v75, v75, v23 quad_perm:[1,0,3,2] row_mask:0xf bank_mask:0xf
	v_fmac_f32_dpp v67, v67, v23 quad_perm:[1,0,3,2] row_mask:0xf bank_mask:0xf

	v_fmac_f32_dpp v58, v58, v24 quad_perm:[2,3,0,1] row_mask:0xf bank_mask:0xf
	v_fmac_f32_dpp v57, v57, v24 quad_perm:[2,3,0,1] row_mask:0xf bank_mask:0xf
	v_fmac_f32_dpp v60, v60, v24 quad_perm:[2,3,0,1] row_mask:0xf bank_mask:0xf
	v_fmac_f32_dpp v62, v62, v24 quad_perm:[2,3,0,1] row_mask:0xf bank_mask:0xf
	v_fmac_f32_dpp v55, v55, v24 quad_perm:[2,3,0,1] row_mask:0xf bank_mask:0xf
	v_fmac_f32_dpp v56, v56, v24 quad_perm:[2,3,0,1] row_mask:0xf bank_mask:0xf
	v_fmac_f32_dpp v61, v61, v24 quad_perm:[2,3,0,1] row_mask:0xf bank_mask:0xf
	v_fmac_f32_dpp v63, v63, v24 quad_perm:[2,3,0,1] row_mask:0xf bank_mask:0xf

	s_or_b32 s22, s10, 3
	v_fmac_f32_dpp v59, v59, v24 quad_perm:[2,3,0,1] row_mask:0xf bank_mask:0xf
	v_fmac_f32_dpp v65, v65, v24 quad_perm:[2,3,0,1] row_mask:0xf bank_mask:0xf
	v_fmac_f32_dpp v70, v70, v24 quad_perm:[2,3,0,1] row_mask:0xf bank_mask:0xf
	v_fmac_f32_dpp v66, v66, v24 quad_perm:[2,3,0,1] row_mask:0xf bank_mask:0xf
	v_fmac_f32_dpp v64, v64, v24 quad_perm:[2,3,0,1] row_mask:0xf bank_mask:0xf
	v_fmac_f32_dpp v69, v69, v24 quad_perm:[2,3,0,1] row_mask:0xf bank_mask:0xf
	v_fmac_f32_dpp v75, v75, v24 quad_perm:[2,3,0,1] row_mask:0xf bank_mask:0xf
	v_fmac_f32_dpp v67, v67, v24 quad_perm:[2,3,0,1] row_mask:0xf bank_mask:0xf

	v_readlane_b32 s19, v52, s18
	v_mov_b32_dpp v68, v58 row_half_mirror row_mask:0xf bank_mask:0xf bound_ctrl:1
	v_mov_b32_dpp v76, v57 row_half_mirror row_mask:0xf bank_mask:0xf bound_ctrl:1
	v_mov_b32_dpp v77, v60 row_half_mirror row_mask:0xf bank_mask:0xf bound_ctrl:1
	v_mov_b32_dpp v78, v62 row_half_mirror row_mask:0xf bank_mask:0xf bound_ctrl:1
	v_mov_b32_dpp v79, v55 row_half_mirror row_mask:0xf bank_mask:0xf bound_ctrl:1
	v_mov_b32_dpp v80, v56 row_half_mirror row_mask:0xf bank_mask:0xf bound_ctrl:1
	v_mov_b32_dpp v81, v61 row_half_mirror row_mask:0xf bank_mask:0xf bound_ctrl:1
	v_mov_b32_dpp v82, v63 row_half_mirror row_mask:0xf bank_mask:0xf bound_ctrl:1
	v_mov_b32_dpp v83, v59 row_half_mirror row_mask:0xf bank_mask:0xf bound_ctrl:1
	v_mov_b32_dpp v84, v65 row_half_mirror row_mask:0xf bank_mask:0xf bound_ctrl:1
	v_mov_b32_dpp v85, v70 row_half_mirror row_mask:0xf bank_mask:0xf bound_ctrl:1
	v_mov_b32_dpp v86, v66 row_half_mirror row_mask:0xf bank_mask:0xf bound_ctrl:1
	v_mov_b32_dpp v87, v64 row_half_mirror row_mask:0xf bank_mask:0xf bound_ctrl:1
	v_mov_b32_dpp v88, v69 row_half_mirror row_mask:0xf bank_mask:0xf bound_ctrl:1
	v_mov_b32_dpp v89, v75 row_half_mirror row_mask:0xf bank_mask:0xf bound_ctrl:1
	v_mov_b32_dpp v90, v67 row_half_mirror row_mask:0xf bank_mask:0xf bound_ctrl:1
	v_fmac_f32_dpp v58, v68, v25 quad_perm:[3,2,1,0] row_mask:0xf bank_mask:0xf
	v_fmac_f32_dpp v57, v76, v25 quad_perm:[3,2,1,0] row_mask:0xf bank_mask:0xf
	v_fmac_f32_dpp v60, v77, v25 quad_perm:[3,2,1,0] row_mask:0xf bank_mask:0xf
	v_fmac_f32_dpp v62, v78, v25 quad_perm:[3,2,1,0] row_mask:0xf bank_mask:0xf
	v_fmac_f32_dpp v55, v79, v25 quad_perm:[3,2,1,0] row_mask:0xf bank_mask:0xf
	v_fmac_f32_dpp v56, v80, v25 quad_perm:[3,2,1,0] row_mask:0xf bank_mask:0xf
	v_fmac_f32_dpp v61, v81, v25 quad_perm:[3,2,1,0] row_mask:0xf bank_mask:0xf
	v_fmac_f32_dpp v63, v82, v25 quad_perm:[3,2,1,0] row_mask:0xf bank_mask:0xf

	v_fmac_f32_dpp v59, v83, v25 quad_perm:[3,2,1,0] row_mask:0xf bank_mask:0xf
	v_fmac_f32_dpp v65, v84, v25 quad_perm:[3,2,1,0] row_mask:0xf bank_mask:0xf
	v_fmac_f32_dpp v70, v85, v25 quad_perm:[3,2,1,0] row_mask:0xf bank_mask:0xf
	v_fmac_f32_dpp v66, v86, v25 quad_perm:[3,2,1,0] row_mask:0xf bank_mask:0xf
	v_fmac_f32_dpp v64, v87, v25 quad_perm:[3,2,1,0] row_mask:0xf bank_mask:0xf
	v_fmac_f32_dpp v69, v88, v25 quad_perm:[3,2,1,0] row_mask:0xf bank_mask:0xf
	v_fmac_f32_dpp v75, v89, v25 quad_perm:[3,2,1,0] row_mask:0xf bank_mask:0xf
	v_fmac_f32_dpp v67, v90, v25 quad_perm:[3,2,1,0] row_mask:0xf bank_mask:0xf

	v_readlane_b32 s18, v52, s22
	s_nop 1
	v_fmac_f32_dpp v58, v58, v26 row_ror:8 row_mask:0xf bank_mask:0xf
	v_fmac_f32_dpp v57, v57, v26 row_ror:8 row_mask:0xf bank_mask:0xf
	v_fmac_f32_dpp v60, v60, v26 row_ror:8 row_mask:0xf bank_mask:0xf
	v_fmac_f32_dpp v62, v62, v26 row_ror:8 row_mask:0xf bank_mask:0xf
	v_fmac_f32_dpp v55, v55, v26 row_ror:8 row_mask:0xf bank_mask:0xf
	v_fmac_f32_dpp v56, v56, v26 row_ror:8 row_mask:0xf bank_mask:0xf
	v_fmac_f32_dpp v61, v61, v26 row_ror:8 row_mask:0xf bank_mask:0xf
	v_fmac_f32_dpp v63, v63, v26 row_ror:8 row_mask:0xf bank_mask:0xf

	v_fmac_f32_dpp v59, v59, v26 row_ror:8 row_mask:0xf bank_mask:0xf
	v_fmac_f32_dpp v65, v65, v26 row_ror:8 row_mask:0xf bank_mask:0xf
	v_fmac_f32_dpp v70, v70, v26 row_ror:8 row_mask:0xf bank_mask:0xf
	v_fmac_f32_dpp v66, v66, v26 row_ror:8 row_mask:0xf bank_mask:0xf
	v_fmac_f32_dpp v64, v64, v26 row_ror:8 row_mask:0xf bank_mask:0xf
	v_fmac_f32_dpp v69, v69, v26 row_ror:8 row_mask:0xf bank_mask:0xf
	v_fmac_f32_dpp v75, v75, v26 row_ror:8 row_mask:0xf bank_mask:0xf
	v_fmac_f32_dpp v67, v67, v26 row_ror:8 row_mask:0xf bank_mask:0xf

	s_or_b32 s23, s10, 2
	v_add_f32 v68, v58, v57
	v_sub_f32 v57, v58, v57
	v_add_f32 v58, v55, v56
	v_sub_f32 v55, v55, v56
	v_add_f32 v56, v60, v62
	v_sub_f32 v60, v60, v62
	v_add_f32 v62, v61, v63
	v_sub_f32 v61, v61, v63
	v_add_f32 v63, v59, v65
	v_sub_f32 v59, v59, v65
	v_add_f32 v65, v64, v69
	v_sub_f32 v64, v64, v69
	v_add_f32 v69, v70, v66
	v_sub_f32 v66, v70, v66
	v_add_f32 v70, v75, v67
	v_sub_f32 v67, v75, v67
	v_add_f32 v75, v68, v56
	v_sub_f32 v56, v68, v56
	v_add_f32 v68, v58, v62
	v_sub_f32 v58, v58, v62
	v_add_f32 v62, v57, v60
	v_sub_f32 v57, v57, v60
	v_add_f32 v60, v55, v61
	v_sub_f32 v55, v55, v61
	v_add_f32 v61, v63, v69
	v_sub_f32 v63, v63, v69
	v_add_f32 v69, v65, v70
	v_sub_f32 v65, v65, v70
	v_add_f32 v70, v59, v66
	v_sub_f32 v59, v59, v66
	v_add_f32 v66, v64, v67
	v_sub_f32 v64, v64, v67
	v_add_f32 v67, v75, v61
	v_sub_f32 v61, v75, v61
	v_add_f32 v75, v68, v69
	v_sub_f32 v68, v68, v69
	v_add_f32 v69, v62, v70
	v_sub_f32 v62, v62, v70
	v_add_f32 v70, v60, v66
	v_sub_f32 v60, v60, v66
	v_add_f32 v66, v56, v63
	v_sub_f32 v56, v56, v63
	v_add_f32 v63, v58, v65
	v_sub_f32 v58, v58, v65
	v_add_f32 v65, v57, v59
	v_sub_f32 v57, v57, v59
	v_add_f32 v59, v55, v64
	v_sub_f32 v55, v55, v64
	v_readlane_b32 s15, v52, s23
	s_nop 1
	v_permlane16_swap_b32 v67, v69
	v_permlane16_swap_b32 v75, v70
	v_permlane16_swap_b32 v66, v65
	v_permlane16_swap_b32 v63, v59
	v_permlane16_swap_b32 v61, v62
	v_permlane16_swap_b32 v68, v60
	v_permlane16_swap_b32 v56, v57
	v_permlane16_swap_b32 v58, v55
	s_or_b32 s24, s10, 5
	v_permlane32_swap_b32 v67, v66
	v_permlane32_swap_b32 v75, v63
	v_permlane32_swap_b32 v69, v65
	v_permlane32_swap_b32 v70, v59
	v_permlane32_swap_b32 v61, v56
	v_permlane32_swap_b32 v68, v58
	v_permlane32_swap_b32 v62, v57
	v_permlane32_swap_b32 v60, v55
	v_readlane_b32 s11, v52, s20
	v_add_f32 v64, v67, v69
	v_sub_f32 v67, v67, v69
	v_add_f32 v69, v75, v70
	v_sub_f32 v70, v75, v70
	v_add_f32 v75, v66, v65
	v_sub_f32 v65, v66, v65
	v_add_f32 v66, v63, v59
	v_sub_f32 v59, v63, v59
	v_add_f32 v63, v61, v62
	v_sub_f32 v61, v61, v62
	v_add_f32 v62, v68, v60
	v_sub_f32 v60, v68, v60
	v_add_f32 v68, v56, v57
	v_sub_f32 v56, v56, v57
	v_add_f32 v57, v58, v55
	v_sub_f32 v55, v58, v55
	v_add_f32 v58, v64, v75
	v_sub_f32 v64, v64, v75
	v_add_f32 v75, v69, v66
	v_sub_f32 v66, v69, v66
	v_add_f32 v69, v67, v65
	v_sub_f32 v65, v67, v65
	v_add_f32 v67, v70, v59
	v_sub_f32 v59, v70, v59
	v_add_f32 v70, v63, v68
	v_sub_f32 v63, v63, v68
	v_add_f32 v68, v62, v57
	v_sub_f32 v57, v62, v57
	v_add_f32 v62, v61, v56
	v_sub_f32 v56, v61, v56
	v_add_f32 v61, v60, v55
	v_sub_f32 v55, v60, v55
	v_mul_f32 v58, v58, v11
	v_mul_f32 v60, v75, v11
	v_mul_f32 v69, v69, v12
	v_mul_f32 v67, v67, v12
	v_mul_f32 v64, v64, v13
	v_mul_f32 v66, v66, v13
	v_mul_f32 v65, v65, v14
	v_mul_f32 v59, v59, v14
	v_mul_f32 v70, v70, v15
	v_mul_f32 v68, v68, v15
	v_mul_f32 v62, v62, v16
	v_mul_f32 v61, v61, v16
	v_mul_f32 v56, v56, v18
	v_mul_f32 v55, v55, v18
	v_mul_f32 v63, v63, v17
	v_mul_f32 v57, v57, v17
	s_nop 0
	v_fma_f32 v75, s19, v67, v58
	v_fma_f32 v76, -s19, v69, v60
	v_fma_f32 v60, s19, v60, v69
	v_fma_f32 v58, -s19, v58, v67
	v_fma_f32 v67, s19, v59, v64
	v_fma_f32 v69, -s19, v65, v66
	v_fma_f32 v65, s19, v66, v65
	v_fma_f32 v59, -s19, v64, v59
	v_fma_f32 v64, s19, v61, v70
	v_fma_f32 v66, -s19, v62, v68
	v_fma_f32 v62, s19, v68, v62
	v_fma_f32 v61, -s19, v70, v61
	v_fma_f32 v68, s19, v55, v63
	v_fma_f32 v70, -s19, v56, v57
	v_fma_f32 v56, s19, v57, v56
	v_fma_f32 v55, -s19, v63, v55
	s_nop 0
	v_fma_f32 v57, s18, v69, v75
	v_fma_f32 v63, -s18, v67, v76
	v_fma_f32 v67, s18, v76, v67
	v_fma_f32 v69, -s18, v75, v69
	v_fma_f32 v75, s18, v59, v60
	v_fma_f32 v76, -s18, v65, v58
	v_fma_f32 v58, s18, v58, v65
	v_fma_f32 v59, -s18, v60, v59
	v_fma_f32 v60, s18, v70, v64
	v_fma_f32 v65, -s18, v68, v66
	v_fma_f32 v66, s18, v66, v68
	v_fma_f32 v64, -s18, v64, v70
	v_fma_f32 v68, s18, v55, v62
	v_fma_f32 v70, -s18, v56, v61
	v_fma_f32 v56, s18, v61, v56
	v_fma_f32 v55, -s18, v62, v55
	s_nop 0
	s_nop 1
	v_permlane32_swap_b32 v57, v67
	v_permlane32_swap_b32 v63, v69
	v_permlane32_swap_b32 v75, v58
	v_permlane32_swap_b32 v76, v59
	s_or_b32 s25, s10, 6
	v_permlane32_swap_b32 v60, v66
	v_permlane32_swap_b32 v65, v64
	v_permlane32_swap_b32 v68, v56
	v_permlane32_swap_b32 v70, v55
	v_permlane16_swap_b32 v57, v75
	v_permlane16_swap_b32 v63, v76
	v_permlane16_swap_b32 v67, v58
	v_permlane16_swap_b32 v69, v59
	s_or_b32 s26, s10, 7
	v_permlane16_swap_b32 v60, v68
	v_permlane16_swap_b32 v65, v70
	v_permlane16_swap_b32 v66, v56
	v_permlane16_swap_b32 v64, v55
	v_fma_f32 v61, s15, v76, v57
	v_fma_f32 v62, -s15, v75, v63
	v_fma_f32 v63, s15, v63, v75
	v_fma_f32 v57, -s15, v57, v76
	v_fma_f32 v75, s15, v59, v67
	v_fma_f32 v76, -s15, v58, v69
	v_fma_f32 v58, s15, v69, v58
	v_fma_f32 v59, -s15, v67, v59
	s_nop 0
	v_fma_f32 v67, s15, v70, v60
	v_fma_f32 v69, -s15, v68, v65
	v_fma_f32 v60, -s15, v60, v70
	v_fma_f32 v70, -s15, v56, v64
	v_fma_f32 v65, s15, v65, v68
	v_fma_f32 v68, s15, v55, v66
	v_fma_f32 v56, s15, v64, v56
	v_fma_f32 v55, -s15, v66, v55
	v_fma_f32 v64, s11, v76, v61
	v_fma_f32 v77, -s11, v75, v62
	v_fma_f32 v75, s11, v62, v75
	v_fma_f32 v61, -s11, v61, v76
	v_fma_f32 v76, s11, v59, v63
	v_fma_f32 v62, -s11, v58, v57
	v_fma_f32 v78, s11, v57, v58
	v_fma_f32 v79, -s11, v63, v59
	s_nop 0
	v_fma_f32 v57, s11, v70, v67
	v_fma_f32 v59, -s11, v68, v69
	v_fma_f32 v69, s11, v69, v68
	v_fma_f32 v70, -s11, v67, v70
	v_fma_f32 v63, s11, v55, v65
	v_readlane_b32 s10, v52, s10
	v_readlane_b32 s20, v52, s24
	v_fma_f32 v80, -s11, v56, v60
	v_fma_f32 v81, s11, v60, v56
	v_fma_f32 v82, -s11, v65, v55
	v_fma_f32 v65, s10, v59, v64
	v_fma_f32 v66, -s10, v57, v77
	v_fma_f32 v58, s10, v77, v57
	v_fma_f32 v59, -s10, v64, v59
	s_nop 0
	v_fma_f32 v67, s10, v80, v76
	v_fma_f32 v68, -s10, v63, v62
	v_fma_f32 v62, s10, v62, v63
	v_fma_f32 v63, -s10, v76, v80
	v_fma_f32 v56, s10, v70, v75
	v_fma_f32 v57, -s10, v69, v61
	v_fma_f32 v55, s10, v61, v69
	v_fma_f32 v64, -s10, v75, v70
	v_fma_f32 v60, s10, v82, v78
	v_fma_f32 v61, -s10, v81, v79
	v_fma_f32 v69, s10, v79, v81
	v_fma_f32 v70, -s10, v78, v82
	s_nop 0
	v_mov_b32_e32 v74, s20
	s_nop 1
	v_mul_f32_dpp v75, v65, v74 row_ror:8 row_mask:0xf bank_mask:0xf
	v_mul_f32_dpp v76, v67, v74 row_ror:8 row_mask:0xf bank_mask:0xf
	v_mul_f32_dpp v77, v56, v74 row_ror:8 row_mask:0xf bank_mask:0xf
	v_mul_f32_dpp v78, v60, v74 row_ror:8 row_mask:0xf bank_mask:0xf
	v_fmac_f32_dpp v65, v66, v74 row_ror:8 row_mask:0xf bank_mask:0xf
	v_fmac_f32_dpp v67, v68, v74 row_ror:8 row_mask:0xf bank_mask:0xf
	v_fmac_f32_dpp v56, v57, v74 row_ror:8 row_mask:0xf bank_mask:0xf
	v_fmac_f32_dpp v60, v61, v74 row_ror:8 row_mask:0xf bank_mask:0xf
	v_sub_f32 v66, v66, v75
	v_sub_f32 v68, v68, v76
	v_sub_f32 v57, v57, v77
	v_sub_f32 v61, v61, v78
	v_readlane_b32 s22, v52, s25
	s_nop 1
	v_mul_f32_dpp v75, v58, v74 row_ror:8 row_mask:0xf bank_mask:0xf
	v_mul_f32_dpp v76, v62, v74 row_ror:8 row_mask:0xf bank_mask:0xf
	v_mul_f32_dpp v77, v55, v74 row_ror:8 row_mask:0xf bank_mask:0xf
	v_mul_f32_dpp v78, v69, v74 row_ror:8 row_mask:0xf bank_mask:0xf
	v_fmac_f32_dpp v58, v59, v74 row_ror:8 row_mask:0xf bank_mask:0xf
	v_fmac_f32_dpp v62, v63, v74 row_ror:8 row_mask:0xf bank_mask:0xf
	v_fmac_f32_dpp v55, v64, v74 row_ror:8 row_mask:0xf bank_mask:0xf
	v_fmac_f32_dpp v69, v70, v74 row_ror:8 row_mask:0xf bank_mask:0xf
	v_sub_f32 v59, v59, v75
	v_sub_f32 v63, v63, v76
	v_sub_f32 v64, v64, v77
	v_sub_f32 v70, v70, v78
	v_readlane_b32 s23, v52, s26
	v_mov_b32_dpp v74, v65 row_half_mirror row_mask:0xf bank_mask:0xf bound_ctrl:1
	v_mov_b32_dpp v75, v67 row_half_mirror row_mask:0xf bank_mask:0xf bound_ctrl:1
	v_mov_b32_dpp v76, v56 row_half_mirror row_mask:0xf bank_mask:0xf bound_ctrl:1
	v_mov_b32_dpp v77, v60 row_half_mirror row_mask:0xf bank_mask:0xf bound_ctrl:1
	v_mov_b32_e32 v73, s22
	v_mov_b32_dpp v78, v66 row_half_mirror row_mask:0xf bank_mask:0xf bound_ctrl:1
	v_mov_b32_dpp v79, v68 row_half_mirror row_mask:0xf bank_mask:0xf bound_ctrl:1
	v_mov_b32_dpp v80, v57 row_half_mirror row_mask:0xf bank_mask:0xf bound_ctrl:1
	v_mov_b32_dpp v81, v61 row_half_mirror row_mask:0xf bank_mask:0xf bound_ctrl:1
	v_mov_b32_dpp v82, v58 row_half_mirror row_mask:0xf bank_mask:0xf bound_ctrl:1
	v_mov_b32_dpp v83, v62 row_half_mirror row_mask:0xf bank_mask:0xf bound_ctrl:1
	v_mov_b32_dpp v84, v55 row_half_mirror row_mask:0xf bank_mask:0xf bound_ctrl:1
	v_mov_b32_dpp v85, v69 row_half_mirror row_mask:0xf bank_mask:0xf bound_ctrl:1
	v_mov_b32_dpp v86, v59 row_half_mirror row_mask:0xf bank_mask:0xf bound_ctrl:1
	v_mov_b32_dpp v87, v63 row_half_mirror row_mask:0xf bank_mask:0xf bound_ctrl:1
	v_mov_b32_dpp v88, v64 row_half_mirror row_mask:0xf bank_mask:0xf bound_ctrl:1
	v_mov_b32_dpp v89, v70 row_half_mirror row_mask:0xf bank_mask:0xf bound_ctrl:1
	v_mul_f32_dpp v90, v74, v73 quad_perm:[3,2,1,0] row_mask:0xf bank_mask:0xf
	v_mul_f32_dpp v91, v75, v73 quad_perm:[3,2,1,0] row_mask:0xf bank_mask:0xf
	v_mul_f32_dpp v92, v76, v73 quad_perm:[3,2,1,0] row_mask:0xf bank_mask:0xf
	v_mul_f32_dpp v93, v77, v73 quad_perm:[3,2,1,0] row_mask:0xf bank_mask:0xf
	v_fmac_f32_dpp v65, v78, v73 quad_perm:[3,2,1,0] row_mask:0xf bank_mask:0xf
	v_fmac_f32_dpp v67, v79, v73 quad_perm:[3,2,1,0] row_mask:0xf bank_mask:0xf
	v_fmac_f32_dpp v56, v80, v73 quad_perm:[3,2,1,0] row_mask:0xf bank_mask:0xf
	v_fmac_f32_dpp v60, v81, v73 quad_perm:[3,2,1,0] row_mask:0xf bank_mask:0xf
	v_sub_f32 v66, v66, v90
	v_sub_f32 v68, v68, v91
	v_sub_f32 v57, v57, v92
	v_sub_f32 v61, v61, v93
	v_mul_f32_dpp v74, v82, v73 quad_perm:[3,2,1,0] row_mask:0xf bank_mask:0xf
	v_mul_f32_dpp v75, v83, v73 quad_perm:[3,2,1,0] row_mask:0xf bank_mask:0xf
	v_mul_f32_dpp v76, v84, v73 quad_perm:[3,2,1,0] row_mask:0xf bank_mask:0xf
	v_mul_f32_dpp v77, v85, v73 quad_perm:[3,2,1,0] row_mask:0xf bank_mask:0xf
	v_fmac_f32_dpp v58, v86, v73 quad_perm:[3,2,1,0] row_mask:0xf bank_mask:0xf
	v_fmac_f32_dpp v62, v87, v73 quad_perm:[3,2,1,0] row_mask:0xf bank_mask:0xf
	v_fmac_f32_dpp v55, v88, v73 quad_perm:[3,2,1,0] row_mask:0xf bank_mask:0xf
	v_fmac_f32_dpp v69, v89, v73 quad_perm:[3,2,1,0] row_mask:0xf bank_mask:0xf
	v_sub_f32 v59, v59, v74
	v_sub_f32 v63, v63, v75
	v_sub_f32 v64, v64, v76
	v_sub_f32 v70, v70, v77
	s_mov_b64 s[8:9], 0
	s_mov_b32 s14, 1
	v_readlane_b32 s21, v52, s21
	s_and_b64 vcc, exec, vcc
	v_mov_b32_e32 v72, s23
	s_nop 1
	v_mul_f32_dpp v73, v65, v72 quad_perm:[2,3,0,1] row_mask:0xf bank_mask:0xf
	v_mul_f32_dpp v74, v67, v72 quad_perm:[2,3,0,1] row_mask:0xf bank_mask:0xf
	v_mul_f32_dpp v75, v56, v72 quad_perm:[2,3,0,1] row_mask:0xf bank_mask:0xf
	v_mul_f32_dpp v76, v60, v72 quad_perm:[2,3,0,1] row_mask:0xf bank_mask:0xf
	v_fmac_f32_dpp v65, v66, v72 quad_perm:[2,3,0,1] row_mask:0xf bank_mask:0xf
	v_fmac_f32_dpp v67, v68, v72 quad_perm:[2,3,0,1] row_mask:0xf bank_mask:0xf
	v_fmac_f32_dpp v56, v57, v72 quad_perm:[2,3,0,1] row_mask:0xf bank_mask:0xf
	v_fmac_f32_dpp v60, v61, v72 quad_perm:[2,3,0,1] row_mask:0xf bank_mask:0xf
	v_sub_f32 v66, v66, v73
	v_sub_f32 v68, v68, v74
	v_sub_f32 v57, v57, v75
	v_sub_f32 v61, v61, v76
	v_mov_b32_e32 v71, s21
	v_mul_f32_dpp v73, v58, v72 quad_perm:[2,3,0,1] row_mask:0xf bank_mask:0xf
	v_mul_f32_dpp v74, v62, v72 quad_perm:[2,3,0,1] row_mask:0xf bank_mask:0xf
	v_mul_f32_dpp v75, v55, v72 quad_perm:[2,3,0,1] row_mask:0xf bank_mask:0xf
	v_mul_f32_dpp v76, v69, v72 quad_perm:[2,3,0,1] row_mask:0xf bank_mask:0xf
	v_fmac_f32_dpp v58, v59, v72 quad_perm:[2,3,0,1] row_mask:0xf bank_mask:0xf
	v_fmac_f32_dpp v62, v63, v72 quad_perm:[2,3,0,1] row_mask:0xf bank_mask:0xf
	v_fmac_f32_dpp v55, v64, v72 quad_perm:[2,3,0,1] row_mask:0xf bank_mask:0xf
	v_fmac_f32_dpp v69, v70, v72 quad_perm:[2,3,0,1] row_mask:0xf bank_mask:0xf
	v_sub_f32 v59, v59, v73
	v_sub_f32 v63, v63, v74
	v_sub_f32 v64, v64, v75
	v_sub_f32 v70, v70, v76
	s_nop 0
	s_nop 1
	v_mul_f32_dpp v72, v65, v71 quad_perm:[1,0,3,2] row_mask:0xf bank_mask:0xf
	v_mul_f32_dpp v73, v67, v71 quad_perm:[1,0,3,2] row_mask:0xf bank_mask:0xf
	v_mul_f32_dpp v74, v56, v71 quad_perm:[1,0,3,2] row_mask:0xf bank_mask:0xf
	v_mul_f32_dpp v75, v60, v71 quad_perm:[1,0,3,2] row_mask:0xf bank_mask:0xf
	v_fmac_f32_dpp v65, v66, v71 quad_perm:[1,0,3,2] row_mask:0xf bank_mask:0xf
	v_fmac_f32_dpp v67, v68, v71 quad_perm:[1,0,3,2] row_mask:0xf bank_mask:0xf
	v_fmac_f32_dpp v56, v57, v71 quad_perm:[1,0,3,2] row_mask:0xf bank_mask:0xf
	v_fmac_f32_dpp v60, v61, v71 quad_perm:[1,0,3,2] row_mask:0xf bank_mask:0xf
	v_sub_f32 v66, v66, v72
	v_sub_f32 v68, v68, v73
	v_sub_f32 v57, v57, v74
	v_sub_f32 v61, v61, v75
	s_nop 0
	s_nop 1
	v_mul_f32_dpp v72, v58, v71 quad_perm:[1,0,3,2] row_mask:0xf bank_mask:0xf
	v_mul_f32_dpp v73, v62, v71 quad_perm:[1,0,3,2] row_mask:0xf bank_mask:0xf
	v_mul_f32_dpp v74, v55, v71 quad_perm:[1,0,3,2] row_mask:0xf bank_mask:0xf
	v_mul_f32_dpp v75, v69, v71 quad_perm:[1,0,3,2] row_mask:0xf bank_mask:0xf
	v_fmac_f32_dpp v58, v59, v71 quad_perm:[1,0,3,2] row_mask:0xf bank_mask:0xf
	v_fmac_f32_dpp v62, v63, v71 quad_perm:[1,0,3,2] row_mask:0xf bank_mask:0xf
	v_fmac_f32_dpp v55, v64, v71 quad_perm:[1,0,3,2] row_mask:0xf bank_mask:0xf
	v_fmac_f32_dpp v69, v70, v71 quad_perm:[1,0,3,2] row_mask:0xf bank_mask:0xf
	v_sub_f32 v59, v59, v72
	v_sub_f32 v63, v63, v73
	v_sub_f32 v64, v64, v74
	v_sub_f32 v70, v70, v75
	s_cbranch_vccz .LBB0_24
	v_mul_f32_e32 v2, v53, v54
	v_mul_f32 v3, v65, v2
	v_mul_f32 v55, v57, v2
	v_mul_f32 v4, v66, v2
	v_mul_f32 v52, v67, v2
	v_mul_f32 v53, v68, v2
	v_mul_f32 v54, v56, v2
	v_mul_f32 v57, v3, v3
	v_mul_f32 v56, v60, v2
	v_mul_f32 v2, v61, v2
	s_mov_b64 s[10:11], 0
	v_fma_f32 v57, v4, v4, v57
	s_nop 0
	v_fma_f32 v57, v52, v52, v57
	s_nop 0
	v_fma_f32 v57, v53, v53, v57
	s_nop 0
	v_fma_f32 v57, v54, v54, v57
	s_nop 0
	v_fma_f32 v57, v55, v55, v57
	s_nop 0
	v_fma_f32 v57, v56, v56, v57
	s_nop 0
	v_fma_f32 v57, v2, v2, v57
	s_nop 1
	v_add_f32_dpp v57, v57, v57 quad_perm:[1,0,3,2] row_mask:0xf bank_mask:0xf bound_ctrl:1
	s_nop 1
	v_add_f32_dpp v57, v57, v57 quad_perm:[2,3,0,1] row_mask:0xf bank_mask:0xf bound_ctrl:1
	ds_swizzle_b32 v58, v57 offset:swizzle(SWAP,4)
	s_waitcnt lgkmcnt(0)
	v_add_f32_e32 v57, v57, v58
	s_nop 1
	v_add_f32_dpp v57, v57, v57 row_ror:8 row_mask:0xf bank_mask:0xf bound_ctrl:1
	ds_swizzle_b32 v58, v57 offset:swizzle(SWAP,16)
	s_waitcnt lgkmcnt(0)
	v_add_f32_e32 v57, v57, v58
	ds_bpermute_b32 v58, v19, v57
	s_waitcnt lgkmcnt(0)
	v_add_f32_e32 v57, v57, v58
	v_mul_f32_e32 v58, 0x4f800000, v57
	v_cmp_gt_f32_e32 vcc, s17, v57
	s_nop 1
	v_cndmask_b32_e32 v57, v57, v58, vcc
	v_sqrt_f32_e32 v58, v57
	s_nop 0
	v_add_u32_e32 v59, -1, v58
	v_add_u32_e32 v60, 1, v58
	v_fma_f32 v61, -v59, v58, v57
	v_fma_f32 v62, -v60, v58, v57
	v_cmp_ge_f32_e64 s[8:9], 0, v61
	s_nop 1
	v_cndmask_b32_e64 v58, v58, v59, s[8:9]
	v_cmp_lt_f32_e64 s[8:9], 0, v62
	s_nop 1
	v_cndmask_b32_e64 v58, v58, v60, s[8:9]
	v_mul_f32_e32 v59, 0x37800000, v58
	v_cndmask_b32_e32 v58, v58, v59, vcc
	v_cmp_class_f32_e32 vcc, v57, v41
	s_nop 1
	v_cndmask_b32_e32 v57, v58, v57, vcc
	v_add_f32_e32 v57, 0x322bcc77, v57
	v_div_scale_f32 v58, s[8:9], v57, v57, 1.0
	v_rcp_f32_e32 v59, v58
	v_div_scale_f32 v60, vcc, 1.0, v57, 1.0
	v_fma_f32 v61, -v58, v59, 1.0
	v_fmac_f32_e32 v59, v61, v59
	v_mul_f32_e32 v61, v60, v59
	v_fma_f32 v62, -v58, v61, v60
	v_fmac_f32_e32 v61, v62, v59
	v_fma_f32 v58, -v58, v61, v60
	v_div_fmas_f32 v58, v58, v59, v61
	v_div_fixup_f32 v57, v58, v57, 1.0
	v_mul_f32 v3, v3, v57
	v_mul_f32 v4, v4, v57
	v_mul_f32 v52, v52, v57
	v_mul_f32 v53, v53, v57
	v_mul_f32 v2, v2, v57
	s_nop 0
	v_mul_f32 v58, v3, v42
	s_nop 0
	v_max_f32 v3, v3, v58
	v_mul_f32 v58, v4, v42
	s_nop 0
	v_max_f32 v4, v4, v58
	v_mul_f32 v58, v52, v42
	s_nop 0
	v_max_f32 v52, v52, v58
	v_mul_f32 v58, v53, v42
	s_nop 0
	v_max_f32 v58, v53, v58
	v_mul_f32 v53, v54, v57
	v_mul_f32 v54, v55, v57
	s_nop 0
	v_mul_f32 v55, v53, v42
	s_nop 0
	v_max_f32 v55, v53, v55
	v_mul_f32 v53, v54, v42
	s_nop 0
	v_max_f32 v59, v54, v53
	v_mul_f32 v53, v56, v57
	s_nop 0
	v_mul_f32 v54, v53, v42
	s_nop 0
	v_max_f32 v60, v53, v54
	v_mul_f32 v53, v2, v42
	s_nop 0
	v_max_f32 v2, v2, v53
	v_mul_f32 v53, v3, v3
	s_nop 0
	v_fma_f32 v53, v4, v4, v53
	s_nop 0
	v_fma_f32 v53, v52, v52, v53
	s_nop 0
	v_fma_f32 v53, v58, v58, v53
	s_nop 0
	v_fma_f32 v53, v55, v55, v53
	s_nop 0
	v_fma_f32 v53, v59, v59, v53
	s_nop 0
	v_fma_f32 v53, v60, v60, v53
	s_nop 0
	v_fma_f32 v53, v2, v2, v53
	s_nop 1
	v_add_f32_dpp v53, v53, v53 quad_perm:[1,0,3,2] row_mask:0xf bank_mask:0xf bound_ctrl:1
	s_nop 1
	v_add_f32_dpp v53, v53, v53 quad_perm:[2,3,0,1] row_mask:0xf bank_mask:0xf bound_ctrl:1
	ds_swizzle_b32 v54, v53 offset:swizzle(SWAP,4)
	s_waitcnt lgkmcnt(0)
	v_add_f32_e32 v53, v53, v54
	s_nop 1
	v_add_f32_dpp v53, v53, v53 row_ror:8 row_mask:0xf bank_mask:0xf bound_ctrl:1
	ds_swizzle_b32 v54, v53 offset:swizzle(SWAP,16)
	s_waitcnt lgkmcnt(0)
	v_add_f32_e32 v53, v53, v54
	ds_bpermute_b32 v54, v19, v53
	s_waitcnt lgkmcnt(0)
	v_add_f32_e32 v53, v53, v54
	v_mul_f32_e32 v54, 0x4f800000, v53
	v_cmp_gt_f32_e32 vcc, s17, v53
	s_nop 1
	v_cndmask_b32_e32 v53, v53, v54, vcc
	v_sqrt_f32_e32 v54, v53
	s_nop 0
	v_add_u32_e32 v56, -1, v54
	v_fma_f32 v57, -v56, v54, v53
	v_cmp_ge_f32_e64 s[8:9], 0, v57
	v_add_u32_e32 v57, 1, v54
	s_nop 0
	v_cndmask_b32_e64 v56, v54, v56, s[8:9]
	v_fma_f32 v54, -v57, v54, v53
	v_cmp_lt_f32_e64 s[8:9], 0, v54
	s_nop 1
	v_cndmask_b32_e64 v54, v56, v57, s[8:9]
	v_mul_f32_e32 v56, 0x37800000, v54
	v_cndmask_b32_e32 v54, v54, v56, vcc
	v_cmp_class_f32_e32 vcc, v53, v41
	s_nop 1
	v_cndmask_b32_e32 v53, v54, v53, vcc
	v_div_scale_f32 v54, s[8:9], v53, v53, 1.0
	v_rcp_f32_e32 v56, v54
	s_nop 0
	v_fma_f32 v57, -v54, v56, 1.0
	v_fmac_f32_e32 v56, v57, v56
	v_div_scale_f32 v57, vcc, 1.0, v53, 1.0
	v_mul_f32_e32 v61, v57, v56
	v_fma_f32 v62, -v54, v61, v57
	v_fmac_f32_e32 v61, v62, v56
	v_fma_f32 v54, -v54, v61, v57
	v_div_fmas_f32 v54, v54, v56, v61
	v_div_fixup_f32 v61, v54, v53, 1.0
	v_mul_f32 v54, v3, v61
	v_mul_f32 v3, v4, v61
	v_mul_f32 v53, v52, v61
	v_mul_f32 v57, v58, v61
	v_mul_f32 v52, v55, v61
	v_mul_f32 v56, v59, v61
	v_mul_f32 v55, v60, v61
	v_mul_f32 v58, v2, v61
	s_branch .LBB0_11
